# P6 epilogue rewrite + tile-contiguous gates, gate loads non-temporal
# speedup vs baseline: 1.0149x; 1.0149x over previous
; __device__ __forceinline__ void unpack8(const v4u w, float (&o)[8]) { o[0] = bflo(w.x); o[1] = bfhi(w.x); o[2] = bflo(w.y); o[3] = bfhi(w.y); o[4] = bflo(w.z); o[5] = bfhi(w.z); o[6] = bflo(w.w); o[7] = bfhi(w.w); }
; __device__ __forceinline__ v4u pack8(const float (&o)[8]) { v4u w; w.x = pk2(o[0], o[1]); w.y = pk2(o[2], o[3]); w.z = pk2(o[4], o[5]); w.w = pk2(o[6], o[7]); return w; }
; __device__ __forceinline__ float sigmf(float x) { return __builtin_amdgcn_rcpf(1.f + __expf(-x)); }
;     __device__ __forceinline__ void operator()(const f32x4 (&acc)[2][2][4][2], const pg8::Unit& u, int wr, int wc, int fr, int fq_in) const {
;         int fq = fq_in; asm volatile("" : "+v"(fq));
;         const int row0 = u.pm * 256 + wr * 64 + fr, col0 = u.pn * 256 + wc * 32 + 8 * fq; const bool first = u.sel == 0; const int goff = first ? 0 : D;
; #pragma unroll
;         for (int bj = 0; bj < 2; ++bj) {
;             const int col = col0 + bj * 128;
;             float b0[8];
;             { const f32x4 t0 = *(const f32x4*)(bg + goff + col), t1 = *(const f32x4*)(bg + goff + col + 4);
; #pragma unroll
;               for (int q = 0; q < 4; ++q) { b0[q] = t0[q]; b0[4 + q] = t1[q]; } }
; #pragma unroll
;             for (int ai = 0; ai < 2; ++ai) {
;                 v4u gw_[4], pw_[4];
; #pragma unroll
;                 for (int m = 0; m < 4; ++m) { const size_t row = (size_t)(row0 + ai * 128 + m * 16);
;                     gw_[m] = *(const v4u*)(Gt + row * (2 * D) + goff + col); pw_[m] = first ? (v4u){0u, 0u, 0u, 0u} : *(const v4u*)(O + row * D + col); }
;                 __builtin_amdgcn_sched_barrier(0);
; #pragma unroll
;                 for (int m = 0; m < 4; ++m) { const size_t row = (size_t)(row0 + ai * 128 + m * 16);
;                     float g0[8], p[8]; unpack8(gw_[m], g0); unpack8(pw_[m], p);
;                     float o[8];
; #pragma unroll
;                     for (int q = 0; q < 4; ++q) { o[q] = p[q] + sigmf(g0[q] + b0[q]) * acc[ai][bj][m][0][q]; o[4 + q] = p[4 + q] + sigmf(g0[4 + q] + b0[4 + q]) * acc[ai][bj][m][1][q]; }
;                     *(v4u*)(O + row * D + col) = pack8(o); }
;             }
.LBB0_903:
	s_lshl_b32 s98, s28, 4
	s_add_i32 s98, s98, s26
	s_cmp_lg_u64 s[30:31], 0
	s_cselect_b32 s99, 8, 0
	s_add_i32 s98, s98, s99
	s_lshl_b32 s98, s98, 17
	s_add_u32 s98, s48, s98
	s_addc_u32 s99, s49, 0
	s_lshl_b32 s8, s28, 20
	s_lshl_b32 s9, s26, 9
	s_add_i32 s8, s8, s9
	s_lshl_b32 s9, s50, 1
	s_add_i32 s8, s8, s9
	v_lshlrev_b32_e32 v226, 12, v216
	v_lshl_add_u32 v226, v1, 4, v226
	v_add_u32_e32 v226, s8, v226
	s_cmp_lg_u64 s[30:31], 0
	s_cselect_b32 s9, 0x2000, 0
	s_lshl_b32 s17, s26, 10
	s_add_i32 s9, s9, s17
	s_lshl_b32 s17, s50, 2
	s_add_i32 s9, s9, s17
	v_lshlrev_b32_e32 v252, 5, v1
	v_add_u32_e32 v252, s9, v252
	v_lshlrev_b32_e32 v227, 4, v0
	s_cmp_lg_u64 s[30:31], 0
	s_cbranch_scc1 .Lepi6_second
	global_load_dwordx4 v[244:247], v252, s[0:1]
	global_load_dwordx4 v[248:251], v252, s[0:1] offset:16
	global_load_dwordx4 v[114:117], v227, s[98:99] nt
	v_add_u32_e32 v254, 0x4000, v227
	global_load_dwordx4 v[118:121], v254, s[98:99] nt
	v_add_u32_e32 v254, 0x8000, v227
	global_load_dwordx4 v[138:141], v254, s[98:99] nt
	v_add_u32_e32 v254, 0xc000, v227
	global_load_dwordx4 v[142:145], v254, s[98:99] nt
	v_add_u32_e32 v254, 0x10000, v227
	global_load_dwordx4 v[146:149], v254, s[98:99] nt
	v_add_u32_e32 v254, 0x14000, v227
	global_load_dwordx4 v[150:153], v254, s[98:99] nt
	v_add_u32_e32 v254, 0x18000, v227
	global_load_dwordx4 v[154:157], v254, s[98:99] nt
	v_add_u32_e32 v254, 0x1c000, v227
	global_load_dwordx4 v[158:161], v254, s[98:99] nt
	v_add_u32_e32 v254, 0x2000, v227
	global_load_dwordx4 v[162:165], v254, s[98:99] nt
	v_add_u32_e32 v254, 0x6000, v227
	global_load_dwordx4 v[166:169], v254, s[98:99] nt
	v_add_u32_e32 v254, 0xa000, v227
	global_load_dwordx4 v[190:193], v254, s[98:99] nt
	v_add_u32_e32 v254, 0xe000, v227
	global_load_dwordx4 v[194:197], v254, s[98:99] nt
	v_add_u32_e32 v254, 0x12000, v227
	global_load_dwordx4 v[198:201], v254, s[98:99] nt
	v_add_u32_e32 v254, 0x16000, v227
	global_load_dwordx4 v[202:205], v254, s[98:99] nt
	v_add_u32_e32 v254, 0x1a000, v227
	global_load_dwordx4 v[206:209], v254, s[98:99] nt
	v_add_u32_e32 v254, 0x1e000, v227
	global_load_dwordx4 v[210:213], v254, s[98:99] nt
	v_mov_b32_e32 v228, 0
	v_mov_b32_e32 v229, 0
	v_mov_b32_e32 v230, 0
	v_mov_b32_e32 v231, 0
	v_mov_b32_e32 v232, 0
	v_mov_b32_e32 v233, 0
	v_mov_b32_e32 v234, 0
	v_mov_b32_e32 v235, 0
	v_mov_b32_e32 v236, 0
	v_mov_b32_e32 v237, 0
	v_mov_b32_e32 v238, 0
	v_mov_b32_e32 v239, 0
	v_mov_b32_e32 v240, 0
	v_mov_b32_e32 v241, 0
	v_mov_b32_e32 v242, 0
	v_mov_b32_e32 v243, 0
	s_waitcnt vmcnt(16)
	s_waitcnt vmcnt(15)
	v_lshlrev_b32_e32 v170, 16, v114
	v_and_b32_e32 v114, 0xffff0000, v114
	v_lshlrev_b32_e32 v171, 16, v115
	v_and_b32_e32 v115, 0xffff0000, v115
	v_lshlrev_b32_e32 v214, 16, v116
	v_and_b32_e32 v116, 0xffff0000, v116
	v_lshlrev_b32_e32 v215, 16, v117
	v_and_b32_e32 v117, 0xffff0000, v117
	v_add_f32_e32 v170, v244, v170
	v_add_f32_e32 v114, v245, v114
	v_add_f32_e32 v171, v246, v171
	v_add_f32_e32 v115, v247, v115
	v_add_f32_e32 v214, v248, v214
	v_add_f32_e32 v116, v249, v116
	v_add_f32_e32 v215, v250, v215
	v_add_f32_e32 v117, v251, v117
	v_mul_f32_e32 v170, 0xbfb8aa3b, v170
	v_mul_f32_e32 v114, 0xbfb8aa3b, v114
	v_mul_f32_e32 v171, 0xbfb8aa3b, v171
	v_mul_f32_e32 v115, 0xbfb8aa3b, v115
	v_mul_f32_e32 v214, 0xbfb8aa3b, v214
	v_mul_f32_e32 v116, 0xbfb8aa3b, v116
	v_mul_f32_e32 v215, 0xbfb8aa3b, v215
	v_mul_f32_e32 v117, 0xbfb8aa3b, v117
	v_exp_f32_e32 v170, v170
	v_exp_f32_e32 v114, v114
	v_exp_f32_e32 v171, v171
	v_exp_f32_e32 v115, v115
	v_exp_f32_e32 v214, v214
	v_exp_f32_e32 v116, v116
	v_exp_f32_e32 v215, v215
	v_exp_f32_e32 v117, v117
	v_add_f32_e32 v170, 1.0, v170
	v_add_f32_e32 v114, 1.0, v114
	v_add_f32_e32 v171, 1.0, v171
	v_add_f32_e32 v115, 1.0, v115
	v_add_f32_e32 v214, 1.0, v214
	v_add_f32_e32 v116, 1.0, v116
	v_add_f32_e32 v215, 1.0, v215
	v_add_f32_e32 v117, 1.0, v117
	v_rcp_f32_e32 v170, v170
	v_rcp_f32_e32 v114, v114
	v_rcp_f32_e32 v171, v171
	v_rcp_f32_e32 v115, v115
	v_rcp_f32_e32 v214, v214
	v_rcp_f32_e32 v116, v116
	v_rcp_f32_e32 v215, v215
	v_rcp_f32_e32 v117, v117
	v_fma_f32 v134, v134, v170, v228
	v_fma_f32 v135, v135, v114, v228
	v_fma_f32 v136, v136, v171, v228
	v_fma_f32 v137, v137, v115, v228
	v_fma_f32 v130, v130, v214, v228
	v_fma_f32 v131, v131, v116, v228
	v_fma_f32 v132, v132, v215, v228
	v_fma_f32 v133, v133, v117, v228
	v_cvt_pk_bf16_f32 v134, v134, v135
	v_cvt_pk_bf16_f32 v135, v136, v137
	v_cvt_pk_bf16_f32 v136, v130, v131
	v_cvt_pk_bf16_f32 v137, v132, v133
	global_store_dwordx4 v226, v[134:137], s[4:5]
	s_waitcnt vmcnt(15)
	v_lshlrev_b32_e32 v170, 16, v118
	v_and_b32_e32 v118, 0xffff0000, v118
	v_lshlrev_b32_e32 v171, 16, v119
	v_and_b32_e32 v119, 0xffff0000, v119
	v_lshlrev_b32_e32 v214, 16, v120
	v_and_b32_e32 v120, 0xffff0000, v120
	v_lshlrev_b32_e32 v215, 16, v121
	v_and_b32_e32 v121, 0xffff0000, v121
	v_add_f32_e32 v170, v244, v170
	v_add_f32_e32 v118, v245, v118
	v_add_f32_e32 v171, v246, v171
	v_add_f32_e32 v119, v247, v119
	v_add_f32_e32 v214, v248, v214
	v_add_f32_e32 v120, v249, v120
	v_add_f32_e32 v215, v250, v215
	v_add_f32_e32 v121, v251, v121
	v_mul_f32_e32 v170, 0xbfb8aa3b, v170
	v_mul_f32_e32 v118, 0xbfb8aa3b, v118
	v_mul_f32_e32 v171, 0xbfb8aa3b, v171
	v_mul_f32_e32 v119, 0xbfb8aa3b, v119
	v_mul_f32_e32 v214, 0xbfb8aa3b, v214
	v_mul_f32_e32 v120, 0xbfb8aa3b, v120
	v_mul_f32_e32 v215, 0xbfb8aa3b, v215
	v_mul_f32_e32 v121, 0xbfb8aa3b, v121
	v_exp_f32_e32 v170, v170
	v_exp_f32_e32 v118, v118
	v_exp_f32_e32 v171, v171
	v_exp_f32_e32 v119, v119
	v_exp_f32_e32 v214, v214
	v_exp_f32_e32 v120, v120
	v_exp_f32_e32 v215, v215
	v_exp_f32_e32 v121, v121
	v_add_f32_e32 v170, 1.0, v170
	v_add_f32_e32 v118, 1.0, v118
	v_add_f32_e32 v171, 1.0, v171
	v_add_f32_e32 v119, 1.0, v119
	v_add_f32_e32 v214, 1.0, v214
	v_add_f32_e32 v120, 1.0, v120
	v_add_f32_e32 v215, 1.0, v215
	v_add_f32_e32 v121, 1.0, v121
	v_rcp_f32_e32 v170, v170
	v_rcp_f32_e32 v118, v118
	v_rcp_f32_e32 v171, v171
	v_rcp_f32_e32 v119, v119
	v_rcp_f32_e32 v214, v214
	v_rcp_f32_e32 v120, v120
	v_rcp_f32_e32 v215, v215
	v_rcp_f32_e32 v121, v121
	v_fma_f32 v126, v126, v170, v232
	v_fma_f32 v127, v127, v118, v232
	v_fma_f32 v128, v128, v171, v232
	v_fma_f32 v129, v129, v119, v232
	v_fma_f32 v122, v122, v214, v232
	v_fma_f32 v123, v123, v120, v232
	v_fma_f32 v124, v124, v215, v232
	v_fma_f32 v125, v125, v121, v232
	v_cvt_pk_bf16_f32 v126, v126, v127
	v_cvt_pk_bf16_f32 v127, v128, v129
	v_cvt_pk_bf16_f32 v128, v122, v123
	v_cvt_pk_bf16_f32 v129, v124, v125
	v_add_u32_e32 v225, 0x10000, v226
	global_store_dwordx4 v225, v[126:129], s[4:5]
	global_load_dwordx4 v[130:133], v252, s[0:1] offset:512
	global_load_dwordx4 v[122:125], v252, s[0:1] offset:528
	s_waitcnt vmcnt(17)
; __device__ __forceinline__ void unpack8(const v4u w, float (&o)[8]) { o[0] = bflo(w.x); o[1] = bfhi(w.x); o[2] = bflo(w.y); o[3] = bfhi(w.y); o[4] = bflo(w.z); o[5] = bfhi(w.z); o[6] = bflo(w.w); o[7] = bfhi(w.w); }
; __device__ __forceinline__ v4u pack8(const float (&o)[8]) { v4u w; w.x = pk2(o[0], o[1]); w.y = pk2(o[2], o[3]); w.z = pk2(o[4], o[5]); w.w = pk2(o[6], o[7]); return w; }
; __device__ __forceinline__ float sigmf(float x) { return __builtin_amdgcn_rcpf(1.f + __expf(-x)); }
;     __device__ __forceinline__ void operator()(const f32x4 (&acc)[2][2][4][2], const pg8::Unit& u, int wr, int wc, int fr, int fq_in) const {
;     ...
;                 for (int m = 0; m < 4; ++m) { const size_t row = (size_t)(row0 + ai * 128 + m * 16);
;                     float g0[8], p[8]; unpack8(gw_[m], g0); unpack8(pw_[m], p);
;                     float o[8];
; #pragma unroll
;                     for (int q = 0; q < 4; ++q) { o[q] = p[q] + sigmf(g0[q] + b0[q]) * acc[ai][bj][m][0][q]; o[4 + q] = p[4 + q] + sigmf(g0[4 + q] + b0[4 + q]) * acc[ai][bj][m][1][q]; }
;                     *(v4u*)(O + row * D + col) = pack8(o); }
	v_lshlrev_b32_e32 v170, 16, v138
	v_and_b32_e32 v138, 0xffff0000, v138
	v_lshlrev_b32_e32 v171, 16, v139
	v_and_b32_e32 v139, 0xffff0000, v139
	v_lshlrev_b32_e32 v214, 16, v140
	v_and_b32_e32 v140, 0xffff0000, v140
	v_lshlrev_b32_e32 v215, 16, v141
	v_and_b32_e32 v141, 0xffff0000, v141
	v_add_f32_e32 v170, v244, v170
	v_add_f32_e32 v138, v245, v138
	v_add_f32_e32 v171, v246, v171
	v_add_f32_e32 v139, v247, v139
	v_add_f32_e32 v214, v248, v214
	v_add_f32_e32 v140, v249, v140
	v_add_f32_e32 v215, v250, v215
	v_add_f32_e32 v141, v251, v141
	v_mul_f32_e32 v170, 0xbfb8aa3b, v170
	v_mul_f32_e32 v138, 0xbfb8aa3b, v138
	v_mul_f32_e32 v171, 0xbfb8aa3b, v171
	v_mul_f32_e32 v139, 0xbfb8aa3b, v139
	v_mul_f32_e32 v214, 0xbfb8aa3b, v214
	v_mul_f32_e32 v140, 0xbfb8aa3b, v140
	v_mul_f32_e32 v215, 0xbfb8aa3b, v215
	v_mul_f32_e32 v141, 0xbfb8aa3b, v141
	v_exp_f32_e32 v170, v170
	v_exp_f32_e32 v138, v138
	v_exp_f32_e32 v171, v171
	v_exp_f32_e32 v139, v139
	v_exp_f32_e32 v214, v214
	v_exp_f32_e32 v140, v140
	v_exp_f32_e32 v215, v215
	v_exp_f32_e32 v141, v141
	v_add_f32_e32 v170, 1.0, v170
	v_add_f32_e32 v138, 1.0, v138
	v_add_f32_e32 v171, 1.0, v171
	v_add_f32_e32 v139, 1.0, v139
	v_add_f32_e32 v214, 1.0, v214
	v_add_f32_e32 v140, 1.0, v140
	v_add_f32_e32 v215, 1.0, v215
	v_add_f32_e32 v141, 1.0, v141
	v_rcp_f32_e32 v170, v170
	v_rcp_f32_e32 v138, v138
	v_rcp_f32_e32 v171, v171
	v_rcp_f32_e32 v139, v139
	v_rcp_f32_e32 v214, v214
	v_rcp_f32_e32 v140, v140
	v_rcp_f32_e32 v215, v215
	v_rcp_f32_e32 v141, v141
	v_fma_f32 v110, v110, v170, v236
	v_fma_f32 v111, v111, v138, v236
	v_fma_f32 v112, v112, v171, v236
	v_fma_f32 v113, v113, v139, v236
	v_fma_f32 v106, v106, v214, v236
	v_fma_f32 v107, v107, v140, v236
	v_fma_f32 v108, v108, v215, v236
	v_fma_f32 v109, v109, v141, v236
	v_cvt_pk_bf16_f32 v110, v110, v111
	v_cvt_pk_bf16_f32 v111, v112, v113
	v_cvt_pk_bf16_f32 v112, v106, v107
	v_cvt_pk_bf16_f32 v113, v108, v109
	v_add_u32_e32 v225, 0x20000, v226
	global_store_dwordx4 v225, v[110:113], s[4:5]
	s_waitcnt vmcnt(17)
	v_lshlrev_b32_e32 v170, 16, v142
	v_and_b32_e32 v142, 0xffff0000, v142
	v_lshlrev_b32_e32 v171, 16, v143
	v_and_b32_e32 v143, 0xffff0000, v143
	v_lshlrev_b32_e32 v214, 16, v144
	v_and_b32_e32 v144, 0xffff0000, v144
	v_lshlrev_b32_e32 v215, 16, v145
	v_and_b32_e32 v145, 0xffff0000, v145
	v_add_f32_e32 v170, v244, v170
	v_add_f32_e32 v142, v245, v142
	v_add_f32_e32 v171, v246, v171
	v_add_f32_e32 v143, v247, v143
	v_add_f32_e32 v214, v248, v214
	v_add_f32_e32 v144, v249, v144
	v_add_f32_e32 v215, v250, v215
	v_add_f32_e32 v145, v251, v145
	v_mul_f32_e32 v170, 0xbfb8aa3b, v170
	v_mul_f32_e32 v142, 0xbfb8aa3b, v142
	v_mul_f32_e32 v171, 0xbfb8aa3b, v171
	v_mul_f32_e32 v143, 0xbfb8aa3b, v143
	v_mul_f32_e32 v214, 0xbfb8aa3b, v214
	v_mul_f32_e32 v144, 0xbfb8aa3b, v144
	v_mul_f32_e32 v215, 0xbfb8aa3b, v215
	v_mul_f32_e32 v145, 0xbfb8aa3b, v145
	v_exp_f32_e32 v170, v170
	v_exp_f32_e32 v142, v142
	v_exp_f32_e32 v171, v171
	v_exp_f32_e32 v143, v143
	v_exp_f32_e32 v214, v214
	v_exp_f32_e32 v144, v144
	v_exp_f32_e32 v215, v215
	v_exp_f32_e32 v145, v145
	v_add_f32_e32 v170, 1.0, v170
	v_add_f32_e32 v142, 1.0, v142
	v_add_f32_e32 v171, 1.0, v171
	v_add_f32_e32 v143, 1.0, v143
	v_add_f32_e32 v214, 1.0, v214
	v_add_f32_e32 v144, 1.0, v144
	v_add_f32_e32 v215, 1.0, v215
	v_add_f32_e32 v145, 1.0, v145
	v_rcp_f32_e32 v170, v170
	v_rcp_f32_e32 v142, v142
	v_rcp_f32_e32 v171, v171
	v_rcp_f32_e32 v143, v143
	v_rcp_f32_e32 v214, v214
	v_rcp_f32_e32 v144, v144
	v_rcp_f32_e32 v215, v215
	v_rcp_f32_e32 v145, v145
	v_fma_f32 v102, v102, v170, v240
	v_fma_f32 v103, v103, v142, v240
	v_fma_f32 v104, v104, v171, v240
	v_fma_f32 v105, v105, v143, v240
	v_fma_f32 v98, v98, v214, v240
	v_fma_f32 v99, v99, v144, v240
	v_fma_f32 v100, v100, v215, v240
	v_fma_f32 v101, v101, v145, v240
	v_cvt_pk_bf16_f32 v102, v102, v103
	v_cvt_pk_bf16_f32 v103, v104, v105
	v_cvt_pk_bf16_f32 v104, v98, v99
	v_cvt_pk_bf16_f32 v105, v100, v101
	v_add_u32_e32 v225, 0x30000, v226
	global_store_dwordx4 v225, v[102:105], s[4:5]
	s_waitcnt vmcnt(17)
	v_lshlrev_b32_e32 v170, 16, v146
	v_and_b32_e32 v146, 0xffff0000, v146
	v_lshlrev_b32_e32 v171, 16, v147
	v_and_b32_e32 v147, 0xffff0000, v147
	v_lshlrev_b32_e32 v214, 16, v148
	v_and_b32_e32 v148, 0xffff0000, v148
	v_lshlrev_b32_e32 v215, 16, v149
	v_and_b32_e32 v149, 0xffff0000, v149
	v_add_f32_e32 v170, v244, v170
	v_add_f32_e32 v146, v245, v146
	v_add_f32_e32 v171, v246, v171
	v_add_f32_e32 v147, v247, v147
	v_add_f32_e32 v214, v248, v214
	v_add_f32_e32 v148, v249, v148
	v_add_f32_e32 v215, v250, v215
	v_add_f32_e32 v149, v251, v149
	v_mul_f32_e32 v170, 0xbfb8aa3b, v170
	v_mul_f32_e32 v146, 0xbfb8aa3b, v146
	v_mul_f32_e32 v171, 0xbfb8aa3b, v171
	v_mul_f32_e32 v147, 0xbfb8aa3b, v147
	v_mul_f32_e32 v214, 0xbfb8aa3b, v214
	v_mul_f32_e32 v148, 0xbfb8aa3b, v148
	v_mul_f32_e32 v215, 0xbfb8aa3b, v215
	v_mul_f32_e32 v149, 0xbfb8aa3b, v149
	v_exp_f32_e32 v170, v170
	v_exp_f32_e32 v146, v146
	v_exp_f32_e32 v171, v171
	v_exp_f32_e32 v147, v147
	v_exp_f32_e32 v214, v214
	v_exp_f32_e32 v148, v148
	v_exp_f32_e32 v215, v215
	v_exp_f32_e32 v149, v149
	v_add_f32_e32 v170, 1.0, v170
	v_add_f32_e32 v146, 1.0, v146
	v_add_f32_e32 v171, 1.0, v171
	v_add_f32_e32 v147, 1.0, v147
	v_add_f32_e32 v214, 1.0, v214
	v_add_f32_e32 v148, 1.0, v148
	v_add_f32_e32 v215, 1.0, v215
	v_add_f32_e32 v149, 1.0, v149
	v_rcp_f32_e32 v170, v170
	v_rcp_f32_e32 v146, v146
	v_rcp_f32_e32 v171, v171
	v_rcp_f32_e32 v147, v147
	v_rcp_f32_e32 v214, v214
	v_rcp_f32_e32 v148, v148
	v_rcp_f32_e32 v215, v215
	v_rcp_f32_e32 v149, v149
	v_fma_f32 v94, v94, v170, v228
	v_fma_f32 v95, v95, v146, v228
	v_fma_f32 v96, v96, v171, v228
	v_fma_f32 v97, v97, v147, v228
	v_fma_f32 v90, v90, v214, v228
	v_fma_f32 v91, v91, v148, v228
	v_fma_f32 v92, v92, v215, v228
	v_fma_f32 v93, v93, v149, v228
	v_cvt_pk_bf16_f32 v94, v94, v95
	v_cvt_pk_bf16_f32 v95, v96, v97
	v_cvt_pk_bf16_f32 v96, v90, v91
	v_cvt_pk_bf16_f32 v97, v92, v93
	v_add_u32_e32 v225, 0x80000, v226
	global_store_dwordx4 v225, v[94:97], s[4:5]
	s_waitcnt vmcnt(17)
; __device__ __forceinline__ void unpack8(const v4u w, float (&o)[8]) { o[0] = bflo(w.x); o[1] = bfhi(w.x); o[2] = bflo(w.y); o[3] = bfhi(w.y); o[4] = bflo(w.z); o[5] = bfhi(w.z); o[6] = bflo(w.w); o[7] = bfhi(w.w); }
; __device__ __forceinline__ v4u pack8(const float (&o)[8]) { v4u w; w.x = pk2(o[0], o[1]); w.y = pk2(o[2], o[3]); w.z = pk2(o[4], o[5]); w.w = pk2(o[6], o[7]); return w; }
; __device__ __forceinline__ float sigmf(float x) { return __builtin_amdgcn_rcpf(1.f + __expf(-x)); }
;     __device__ __forceinline__ void operator()(const f32x4 (&acc)[2][2][4][2], const pg8::Unit& u, int wr, int wc, int fr, int fq_in) const {
;     ...
;                 for (int m = 0; m < 4; ++m) { const size_t row = (size_t)(row0 + ai * 128 + m * 16);
;                     gw_[m] = *(const v4u*)(Gt + row * (2 * D) + goff + col); pw_[m] = first ? (v4u){0u, 0u, 0u, 0u} : *(const v4u*)(O + row * D + col); }
;                 __builtin_amdgcn_sched_barrier(0);
; #pragma unroll
;                 for (int m = 0; m < 4; ++m) { const size_t row = (size_t)(row0 + ai * 128 + m * 16);
;                     float g0[8], p[8]; unpack8(gw_[m], g0); unpack8(pw_[m], p);
;                     float o[8];
; #pragma unroll
;                     for (int q = 0; q < 4; ++q) { o[q] = p[q] + sigmf(g0[q] + b0[q]) * acc[ai][bj][m][0][q]; o[4 + q] = p[4 + q] + sigmf(g0[4 + q] + b0[4 + q]) * acc[ai][bj][m][1][q]; }
;                     *(v4u*)(O + row * D + col) = pack8(o); }
	v_lshlrev_b32_e32 v170, 16, v150
	v_and_b32_e32 v150, 0xffff0000, v150
	v_lshlrev_b32_e32 v171, 16, v151
	v_and_b32_e32 v151, 0xffff0000, v151
	v_lshlrev_b32_e32 v214, 16, v152
	v_and_b32_e32 v152, 0xffff0000, v152
	v_lshlrev_b32_e32 v215, 16, v153
	v_and_b32_e32 v153, 0xffff0000, v153
	v_add_f32_e32 v170, v244, v170
	v_add_f32_e32 v150, v245, v150
	v_add_f32_e32 v171, v246, v171
	v_add_f32_e32 v151, v247, v151
	v_add_f32_e32 v214, v248, v214
	v_add_f32_e32 v152, v249, v152
	v_add_f32_e32 v215, v250, v215
	v_add_f32_e32 v153, v251, v153
	v_mul_f32_e32 v170, 0xbfb8aa3b, v170
	v_mul_f32_e32 v150, 0xbfb8aa3b, v150
	v_mul_f32_e32 v171, 0xbfb8aa3b, v171
	v_mul_f32_e32 v151, 0xbfb8aa3b, v151
	v_mul_f32_e32 v214, 0xbfb8aa3b, v214
	v_mul_f32_e32 v152, 0xbfb8aa3b, v152
	v_mul_f32_e32 v215, 0xbfb8aa3b, v215
	v_mul_f32_e32 v153, 0xbfb8aa3b, v153
	v_exp_f32_e32 v170, v170
	v_exp_f32_e32 v150, v150
	v_exp_f32_e32 v171, v171
	v_exp_f32_e32 v151, v151
	v_exp_f32_e32 v214, v214
	v_exp_f32_e32 v152, v152
	v_exp_f32_e32 v215, v215
	v_exp_f32_e32 v153, v153
	v_add_f32_e32 v170, 1.0, v170
	v_add_f32_e32 v150, 1.0, v150
	v_add_f32_e32 v171, 1.0, v171
	v_add_f32_e32 v151, 1.0, v151
	v_add_f32_e32 v214, 1.0, v214
	v_add_f32_e32 v152, 1.0, v152
	v_add_f32_e32 v215, 1.0, v215
	v_add_f32_e32 v153, 1.0, v153
	v_rcp_f32_e32 v170, v170
	v_rcp_f32_e32 v150, v150
	v_rcp_f32_e32 v171, v171
	v_rcp_f32_e32 v151, v151
	v_rcp_f32_e32 v214, v214
	v_rcp_f32_e32 v152, v152
	v_rcp_f32_e32 v215, v215
	v_rcp_f32_e32 v153, v153
	v_fma_f32 v86, v86, v170, v232
	v_fma_f32 v87, v87, v150, v232
	v_fma_f32 v88, v88, v171, v232
	v_fma_f32 v89, v89, v151, v232
	v_fma_f32 v82, v82, v214, v232
	v_fma_f32 v83, v83, v152, v232
	v_fma_f32 v84, v84, v215, v232
	v_fma_f32 v85, v85, v153, v232
	v_cvt_pk_bf16_f32 v86, v86, v87
	v_cvt_pk_bf16_f32 v87, v88, v89
	v_cvt_pk_bf16_f32 v88, v82, v83
	v_cvt_pk_bf16_f32 v89, v84, v85
	v_add_u32_e32 v225, 0x90000, v226
	global_store_dwordx4 v225, v[86:89], s[4:5]
	s_waitcnt vmcnt(17)
	v_lshlrev_b32_e32 v170, 16, v154
	v_and_b32_e32 v154, 0xffff0000, v154
	v_lshlrev_b32_e32 v171, 16, v155
	v_and_b32_e32 v155, 0xffff0000, v155
	v_lshlrev_b32_e32 v214, 16, v156
	v_and_b32_e32 v156, 0xffff0000, v156
	v_lshlrev_b32_e32 v215, 16, v157
	v_and_b32_e32 v157, 0xffff0000, v157
	v_add_f32_e32 v170, v244, v170
	v_add_f32_e32 v154, v245, v154
	v_add_f32_e32 v171, v246, v171
	v_add_f32_e32 v155, v247, v155
	v_add_f32_e32 v214, v248, v214
	v_add_f32_e32 v156, v249, v156
	v_add_f32_e32 v215, v250, v215
	v_add_f32_e32 v157, v251, v157
	v_mul_f32_e32 v170, 0xbfb8aa3b, v170
	v_mul_f32_e32 v154, 0xbfb8aa3b, v154
	v_mul_f32_e32 v171, 0xbfb8aa3b, v171
	v_mul_f32_e32 v155, 0xbfb8aa3b, v155
	v_mul_f32_e32 v214, 0xbfb8aa3b, v214
	v_mul_f32_e32 v156, 0xbfb8aa3b, v156
	v_mul_f32_e32 v215, 0xbfb8aa3b, v215
	v_mul_f32_e32 v157, 0xbfb8aa3b, v157
	v_exp_f32_e32 v170, v170
	v_exp_f32_e32 v154, v154
	v_exp_f32_e32 v171, v171
	v_exp_f32_e32 v155, v155
	v_exp_f32_e32 v214, v214
	v_exp_f32_e32 v156, v156
	v_exp_f32_e32 v215, v215
	v_exp_f32_e32 v157, v157
	v_add_f32_e32 v170, 1.0, v170
	v_add_f32_e32 v154, 1.0, v154
	v_add_f32_e32 v171, 1.0, v171
	v_add_f32_e32 v155, 1.0, v155
	v_add_f32_e32 v214, 1.0, v214
	v_add_f32_e32 v156, 1.0, v156
	v_add_f32_e32 v215, 1.0, v215
	v_add_f32_e32 v157, 1.0, v157
	v_rcp_f32_e32 v170, v170
	v_rcp_f32_e32 v154, v154
	v_rcp_f32_e32 v171, v171
	v_rcp_f32_e32 v155, v155
	v_rcp_f32_e32 v214, v214
	v_rcp_f32_e32 v156, v156
	v_rcp_f32_e32 v215, v215
	v_rcp_f32_e32 v157, v157
	v_fma_f32 v78, v78, v170, v236
	v_fma_f32 v79, v79, v154, v236
	v_fma_f32 v80, v80, v171, v236
	v_fma_f32 v81, v81, v155, v236
	v_fma_f32 v74, v74, v214, v236
	v_fma_f32 v75, v75, v156, v236
	v_fma_f32 v76, v76, v215, v236
	v_fma_f32 v77, v77, v157, v236
	v_cvt_pk_bf16_f32 v78, v78, v79
	v_cvt_pk_bf16_f32 v79, v80, v81
	v_cvt_pk_bf16_f32 v80, v74, v75
	v_cvt_pk_bf16_f32 v81, v76, v77
	v_add_u32_e32 v225, 0xa0000, v226
	global_store_dwordx4 v225, v[78:81], s[4:5]
	s_waitcnt vmcnt(17)
	v_lshlrev_b32_e32 v170, 16, v158
	v_and_b32_e32 v158, 0xffff0000, v158
	v_lshlrev_b32_e32 v171, 16, v159
	v_and_b32_e32 v159, 0xffff0000, v159
	v_lshlrev_b32_e32 v214, 16, v160
	v_and_b32_e32 v160, 0xffff0000, v160
	v_lshlrev_b32_e32 v215, 16, v161
	v_and_b32_e32 v161, 0xffff0000, v161
	v_add_f32_e32 v170, v244, v170
	v_add_f32_e32 v158, v245, v158
	v_add_f32_e32 v171, v246, v171
	v_add_f32_e32 v159, v247, v159
	v_add_f32_e32 v214, v248, v214
	v_add_f32_e32 v160, v249, v160
	v_add_f32_e32 v215, v250, v215
	v_add_f32_e32 v161, v251, v161
	v_mul_f32_e32 v170, 0xbfb8aa3b, v170
	v_mul_f32_e32 v158, 0xbfb8aa3b, v158
	v_mul_f32_e32 v171, 0xbfb8aa3b, v171
	v_mul_f32_e32 v159, 0xbfb8aa3b, v159
	v_mul_f32_e32 v214, 0xbfb8aa3b, v214
	v_mul_f32_e32 v160, 0xbfb8aa3b, v160
	v_mul_f32_e32 v215, 0xbfb8aa3b, v215
	v_mul_f32_e32 v161, 0xbfb8aa3b, v161
	v_exp_f32_e32 v170, v170
	v_exp_f32_e32 v158, v158
	v_exp_f32_e32 v171, v171
	v_exp_f32_e32 v159, v159
	v_exp_f32_e32 v214, v214
	v_exp_f32_e32 v160, v160
	v_exp_f32_e32 v215, v215
	v_exp_f32_e32 v161, v161
	v_add_f32_e32 v170, 1.0, v170
	v_add_f32_e32 v158, 1.0, v158
	v_add_f32_e32 v171, 1.0, v171
	v_add_f32_e32 v159, 1.0, v159
	v_add_f32_e32 v214, 1.0, v214
	v_add_f32_e32 v160, 1.0, v160
	v_add_f32_e32 v215, 1.0, v215
	v_add_f32_e32 v161, 1.0, v161
	v_rcp_f32_e32 v170, v170
	v_rcp_f32_e32 v158, v158
	v_rcp_f32_e32 v171, v171
	v_rcp_f32_e32 v159, v159
	v_rcp_f32_e32 v214, v214
	v_rcp_f32_e32 v160, v160
	v_rcp_f32_e32 v215, v215
	v_rcp_f32_e32 v161, v161
	v_fma_f32 v70, v70, v170, v240
	v_fma_f32 v71, v71, v158, v240
	v_fma_f32 v72, v72, v171, v240
	v_fma_f32 v73, v73, v159, v240
	v_fma_f32 v66, v66, v214, v240
	v_fma_f32 v67, v67, v160, v240
	v_fma_f32 v68, v68, v215, v240
	v_fma_f32 v69, v69, v161, v240
	v_cvt_pk_bf16_f32 v70, v70, v71
	v_cvt_pk_bf16_f32 v71, v72, v73
	v_cvt_pk_bf16_f32 v72, v66, v67
	v_cvt_pk_bf16_f32 v73, v68, v69
	v_add_u32_e32 v225, 0xb0000, v226
	global_store_dwordx4 v225, v[70:73], s[4:5]
	s_waitcnt vmcnt(6)
; __device__ __forceinline__ void unpack8(const v4u w, float (&o)[8]) { o[0] = bflo(w.x); o[1] = bfhi(w.x); o[2] = bflo(w.y); o[3] = bfhi(w.y); o[4] = bflo(w.z); o[5] = bfhi(w.z); o[6] = bflo(w.w); o[7] = bfhi(w.w); }
; __device__ __forceinline__ v4u pack8(const float (&o)[8]) { v4u w; w.x = pk2(o[0], o[1]); w.y = pk2(o[2], o[3]); w.z = pk2(o[4], o[5]); w.w = pk2(o[6], o[7]); return w; }
; __device__ __forceinline__ float sigmf(float x) { return __builtin_amdgcn_rcpf(1.f + __expf(-x)); }
;     __device__ __forceinline__ void operator()(const f32x4 (&acc)[2][2][4][2], const pg8::Unit& u, int wr, int wc, int fr, int fq_in) const {
;     ...
;                 for (int m = 0; m < 4; ++m) { const size_t row = (size_t)(row0 + ai * 128 + m * 16);
;                     gw_[m] = *(const v4u*)(Gt + row * (2 * D) + goff + col); pw_[m] = first ? (v4u){0u, 0u, 0u, 0u} : *(const v4u*)(O + row * D + col); }
;                 __builtin_amdgcn_sched_barrier(0);
; #pragma unroll
;                 for (int m = 0; m < 4; ++m) { const size_t row = (size_t)(row0 + ai * 128 + m * 16);
;                     float g0[8], p[8]; unpack8(gw_[m], g0); unpack8(pw_[m], p);
;                     float o[8];
; #pragma unroll
;                     for (int q = 0; q < 4; ++q) { o[q] = p[q] + sigmf(g0[q] + b0[q]) * acc[ai][bj][m][0][q]; o[4 + q] = p[4 + q] + sigmf(g0[4 + q] + b0[4 + q]) * acc[ai][bj][m][1][q]; }
;                     *(v4u*)(O + row * D + col) = pack8(o); }
	s_waitcnt vmcnt(17)
	v_lshlrev_b32_e32 v170, 16, v162
	v_and_b32_e32 v162, 0xffff0000, v162
	v_lshlrev_b32_e32 v171, 16, v163
	v_and_b32_e32 v163, 0xffff0000, v163
	v_lshlrev_b32_e32 v214, 16, v164
	v_and_b32_e32 v164, 0xffff0000, v164
	v_lshlrev_b32_e32 v215, 16, v165
	v_and_b32_e32 v165, 0xffff0000, v165
	v_add_f32_e32 v170, v130, v170
	v_add_f32_e32 v162, v131, v162
	v_add_f32_e32 v171, v132, v171
	v_add_f32_e32 v163, v133, v163
	v_add_f32_e32 v214, v122, v214
	v_add_f32_e32 v164, v123, v164
	v_add_f32_e32 v215, v124, v215
	v_add_f32_e32 v165, v125, v165
	v_mul_f32_e32 v170, 0xbfb8aa3b, v170
	v_mul_f32_e32 v162, 0xbfb8aa3b, v162
	v_mul_f32_e32 v171, 0xbfb8aa3b, v171
	v_mul_f32_e32 v163, 0xbfb8aa3b, v163
	v_mul_f32_e32 v214, 0xbfb8aa3b, v214
	v_mul_f32_e32 v164, 0xbfb8aa3b, v164
	v_mul_f32_e32 v215, 0xbfb8aa3b, v215
	v_mul_f32_e32 v165, 0xbfb8aa3b, v165
	v_exp_f32_e32 v170, v170
	v_exp_f32_e32 v162, v162
	v_exp_f32_e32 v171, v171
	v_exp_f32_e32 v163, v163
	v_exp_f32_e32 v214, v214
	v_exp_f32_e32 v164, v164
	v_exp_f32_e32 v215, v215
	v_exp_f32_e32 v165, v165
	v_add_f32_e32 v170, 1.0, v170
	v_add_f32_e32 v162, 1.0, v162
	v_add_f32_e32 v171, 1.0, v171
	v_add_f32_e32 v163, 1.0, v163
	v_add_f32_e32 v214, 1.0, v214
	v_add_f32_e32 v164, 1.0, v164
	v_add_f32_e32 v215, 1.0, v215
	v_add_f32_e32 v165, 1.0, v165
	v_rcp_f32_e32 v170, v170
	v_rcp_f32_e32 v162, v162
	v_rcp_f32_e32 v171, v171
	v_rcp_f32_e32 v163, v163
	v_rcp_f32_e32 v214, v214
	v_rcp_f32_e32 v164, v164
	v_rcp_f32_e32 v215, v215
	v_rcp_f32_e32 v165, v165
	v_fma_f32 v62, v62, v170, v228
	v_fma_f32 v63, v63, v162, v228
	v_fma_f32 v64, v64, v171, v228
	v_fma_f32 v65, v65, v163, v228
	v_fma_f32 v58, v58, v214, v228
	v_fma_f32 v59, v59, v164, v228
	v_fma_f32 v60, v60, v215, v228
	v_fma_f32 v61, v61, v165, v228
	v_cvt_pk_bf16_f32 v62, v62, v63
	v_cvt_pk_bf16_f32 v63, v64, v65
	v_cvt_pk_bf16_f32 v64, v58, v59
	v_cvt_pk_bf16_f32 v65, v60, v61
	global_store_dwordx4 v226, v[62:65], s[4:5] offset:256
	s_waitcnt vmcnt(17)
	v_lshlrev_b32_e32 v170, 16, v166
	v_and_b32_e32 v166, 0xffff0000, v166
	v_lshlrev_b32_e32 v171, 16, v167
	v_and_b32_e32 v167, 0xffff0000, v167
	v_lshlrev_b32_e32 v214, 16, v168
	v_and_b32_e32 v168, 0xffff0000, v168
	v_lshlrev_b32_e32 v215, 16, v169
	v_and_b32_e32 v169, 0xffff0000, v169
	v_add_f32_e32 v170, v130, v170
	v_add_f32_e32 v166, v131, v166
	v_add_f32_e32 v171, v132, v171
	v_add_f32_e32 v167, v133, v167
	v_add_f32_e32 v214, v122, v214
	v_add_f32_e32 v168, v123, v168
	v_add_f32_e32 v215, v124, v215
	v_add_f32_e32 v169, v125, v169
	v_mul_f32_e32 v170, 0xbfb8aa3b, v170
	v_mul_f32_e32 v166, 0xbfb8aa3b, v166
	v_mul_f32_e32 v171, 0xbfb8aa3b, v171
	v_mul_f32_e32 v167, 0xbfb8aa3b, v167
	v_mul_f32_e32 v214, 0xbfb8aa3b, v214
	v_mul_f32_e32 v168, 0xbfb8aa3b, v168
	v_mul_f32_e32 v215, 0xbfb8aa3b, v215
	v_mul_f32_e32 v169, 0xbfb8aa3b, v169
	v_exp_f32_e32 v170, v170
	v_exp_f32_e32 v166, v166
	v_exp_f32_e32 v171, v171
	v_exp_f32_e32 v167, v167
	v_exp_f32_e32 v214, v214
	v_exp_f32_e32 v168, v168
	v_exp_f32_e32 v215, v215
	v_exp_f32_e32 v169, v169
	v_add_f32_e32 v170, 1.0, v170
	v_add_f32_e32 v166, 1.0, v166
	v_add_f32_e32 v171, 1.0, v171
	v_add_f32_e32 v167, 1.0, v167
	v_add_f32_e32 v214, 1.0, v214
	v_add_f32_e32 v168, 1.0, v168
	v_add_f32_e32 v215, 1.0, v215
	v_add_f32_e32 v169, 1.0, v169
	v_rcp_f32_e32 v170, v170
	v_rcp_f32_e32 v166, v166
	v_rcp_f32_e32 v171, v171
	v_rcp_f32_e32 v167, v167
	v_rcp_f32_e32 v214, v214
	v_rcp_f32_e32 v168, v168
	v_rcp_f32_e32 v215, v215
	v_rcp_f32_e32 v169, v169
	v_fma_f32 v54, v54, v170, v232
	v_fma_f32 v55, v55, v166, v232
	v_fma_f32 v56, v56, v171, v232
	v_fma_f32 v57, v57, v167, v232
	v_fma_f32 v50, v50, v214, v232
	v_fma_f32 v51, v51, v168, v232
	v_fma_f32 v52, v52, v215, v232
	v_fma_f32 v53, v53, v169, v232
	v_cvt_pk_bf16_f32 v54, v54, v55
	v_cvt_pk_bf16_f32 v55, v56, v57
	v_cvt_pk_bf16_f32 v56, v50, v51
	v_cvt_pk_bf16_f32 v57, v52, v53
	v_add_u32_e32 v225, 0x10000, v226
	global_store_dwordx4 v225, v[54:57], s[4:5] offset:256
	s_waitcnt vmcnt(17)
	v_lshlrev_b32_e32 v170, 16, v190
	v_and_b32_e32 v190, 0xffff0000, v190
	v_lshlrev_b32_e32 v171, 16, v191
	v_and_b32_e32 v191, 0xffff0000, v191
	v_lshlrev_b32_e32 v214, 16, v192
	v_and_b32_e32 v192, 0xffff0000, v192
	v_lshlrev_b32_e32 v215, 16, v193
	v_and_b32_e32 v193, 0xffff0000, v193
	v_add_f32_e32 v170, v130, v170
	v_add_f32_e32 v190, v131, v190
	v_add_f32_e32 v171, v132, v171
	v_add_f32_e32 v191, v133, v191
	v_add_f32_e32 v214, v122, v214
	v_add_f32_e32 v192, v123, v192
	v_add_f32_e32 v215, v124, v215
	v_add_f32_e32 v193, v125, v193
	v_mul_f32_e32 v170, 0xbfb8aa3b, v170
	v_mul_f32_e32 v190, 0xbfb8aa3b, v190
	v_mul_f32_e32 v171, 0xbfb8aa3b, v171
	v_mul_f32_e32 v191, 0xbfb8aa3b, v191
	v_mul_f32_e32 v214, 0xbfb8aa3b, v214
	v_mul_f32_e32 v192, 0xbfb8aa3b, v192
	v_mul_f32_e32 v215, 0xbfb8aa3b, v215
	v_mul_f32_e32 v193, 0xbfb8aa3b, v193
	v_exp_f32_e32 v170, v170
	v_exp_f32_e32 v190, v190
	v_exp_f32_e32 v171, v171
	v_exp_f32_e32 v191, v191
	v_exp_f32_e32 v214, v214
	v_exp_f32_e32 v192, v192
	v_exp_f32_e32 v215, v215
	v_exp_f32_e32 v193, v193
	v_add_f32_e32 v170, 1.0, v170
	v_add_f32_e32 v190, 1.0, v190
	v_add_f32_e32 v171, 1.0, v171
	v_add_f32_e32 v191, 1.0, v191
	v_add_f32_e32 v214, 1.0, v214
	v_add_f32_e32 v192, 1.0, v192
	v_add_f32_e32 v215, 1.0, v215
	v_add_f32_e32 v193, 1.0, v193
	v_rcp_f32_e32 v170, v170
	v_rcp_f32_e32 v190, v190
	v_rcp_f32_e32 v171, v171
	v_rcp_f32_e32 v191, v191
	v_rcp_f32_e32 v214, v214
	v_rcp_f32_e32 v192, v192
	v_rcp_f32_e32 v215, v215
	v_rcp_f32_e32 v193, v193
	v_fma_f32 v46, v46, v170, v236
	v_fma_f32 v47, v47, v190, v236
	v_fma_f32 v48, v48, v171, v236
	v_fma_f32 v49, v49, v191, v236
	v_fma_f32 v42, v42, v214, v236
	v_fma_f32 v43, v43, v192, v236
	v_fma_f32 v44, v44, v215, v236
	v_fma_f32 v45, v45, v193, v236
	v_cvt_pk_bf16_f32 v46, v46, v47
	v_cvt_pk_bf16_f32 v47, v48, v49
	v_cvt_pk_bf16_f32 v48, v42, v43
	v_cvt_pk_bf16_f32 v49, v44, v45
	v_add_u32_e32 v225, 0x20000, v226
	global_store_dwordx4 v225, v[46:49], s[4:5] offset:256
	s_waitcnt vmcnt(17)
; __device__ __forceinline__ void unpack8(const v4u w, float (&o)[8]) { o[0] = bflo(w.x); o[1] = bfhi(w.x); o[2] = bflo(w.y); o[3] = bfhi(w.y); o[4] = bflo(w.z); o[5] = bfhi(w.z); o[6] = bflo(w.w); o[7] = bfhi(w.w); }
; __device__ __forceinline__ v4u pack8(const float (&o)[8]) { v4u w; w.x = pk2(o[0], o[1]); w.y = pk2(o[2], o[3]); w.z = pk2(o[4], o[5]); w.w = pk2(o[6], o[7]); return w; }
; __device__ __forceinline__ float sigmf(float x) { return __builtin_amdgcn_rcpf(1.f + __expf(-x)); }
;     __device__ __forceinline__ void operator()(const f32x4 (&acc)[2][2][4][2], const pg8::Unit& u, int wr, int wc, int fr, int fq_in) const {
;     ...
;                 for (int m = 0; m < 4; ++m) { const size_t row = (size_t)(row0 + ai * 128 + m * 16);
;                     gw_[m] = *(const v4u*)(Gt + row * (2 * D) + goff + col); pw_[m] = first ? (v4u){0u, 0u, 0u, 0u} : *(const v4u*)(O + row * D + col); }
;                 __builtin_amdgcn_sched_barrier(0);
; #pragma unroll
;                 for (int m = 0; m < 4; ++m) { const size_t row = (size_t)(row0 + ai * 128 + m * 16);
;                     float g0[8], p[8]; unpack8(gw_[m], g0); unpack8(pw_[m], p);
;                     float o[8];
; #pragma unroll
;                     for (int q = 0; q < 4; ++q) { o[q] = p[q] + sigmf(g0[q] + b0[q]) * acc[ai][bj][m][0][q]; o[4 + q] = p[4 + q] + sigmf(g0[4 + q] + b0[4 + q]) * acc[ai][bj][m][1][q]; }
;                     *(v4u*)(O + row * D + col) = pack8(o); }
	v_lshlrev_b32_e32 v170, 16, v194
	v_and_b32_e32 v194, 0xffff0000, v194
	v_lshlrev_b32_e32 v171, 16, v195
	v_and_b32_e32 v195, 0xffff0000, v195
	v_lshlrev_b32_e32 v214, 16, v196
	v_and_b32_e32 v196, 0xffff0000, v196
	v_lshlrev_b32_e32 v215, 16, v197
	v_and_b32_e32 v197, 0xffff0000, v197
	v_add_f32_e32 v170, v130, v170
	v_add_f32_e32 v194, v131, v194
	v_add_f32_e32 v171, v132, v171
	v_add_f32_e32 v195, v133, v195
	v_add_f32_e32 v214, v122, v214
	v_add_f32_e32 v196, v123, v196
	v_add_f32_e32 v215, v124, v215
	v_add_f32_e32 v197, v125, v197
	v_mul_f32_e32 v170, 0xbfb8aa3b, v170
	v_mul_f32_e32 v194, 0xbfb8aa3b, v194
	v_mul_f32_e32 v171, 0xbfb8aa3b, v171
	v_mul_f32_e32 v195, 0xbfb8aa3b, v195
	v_mul_f32_e32 v214, 0xbfb8aa3b, v214
	v_mul_f32_e32 v196, 0xbfb8aa3b, v196
	v_mul_f32_e32 v215, 0xbfb8aa3b, v215
	v_mul_f32_e32 v197, 0xbfb8aa3b, v197
	v_exp_f32_e32 v170, v170
	v_exp_f32_e32 v194, v194
	v_exp_f32_e32 v171, v171
	v_exp_f32_e32 v195, v195
	v_exp_f32_e32 v214, v214
	v_exp_f32_e32 v196, v196
	v_exp_f32_e32 v215, v215
	v_exp_f32_e32 v197, v197
	v_add_f32_e32 v170, 1.0, v170
	v_add_f32_e32 v194, 1.0, v194
	v_add_f32_e32 v171, 1.0, v171
	v_add_f32_e32 v195, 1.0, v195
	v_add_f32_e32 v214, 1.0, v214
	v_add_f32_e32 v196, 1.0, v196
	v_add_f32_e32 v215, 1.0, v215
	v_add_f32_e32 v197, 1.0, v197
	v_rcp_f32_e32 v170, v170
	v_rcp_f32_e32 v194, v194
	v_rcp_f32_e32 v171, v171
	v_rcp_f32_e32 v195, v195
	v_rcp_f32_e32 v214, v214
	v_rcp_f32_e32 v196, v196
	v_rcp_f32_e32 v215, v215
	v_rcp_f32_e32 v197, v197
	v_fma_f32 v38, v38, v170, v240
	v_fma_f32 v39, v39, v194, v240
	v_fma_f32 v40, v40, v171, v240
	v_fma_f32 v41, v41, v195, v240
	v_fma_f32 v34, v34, v214, v240
	v_fma_f32 v35, v35, v196, v240
	v_fma_f32 v36, v36, v215, v240
	v_fma_f32 v37, v37, v197, v240
	v_cvt_pk_bf16_f32 v38, v38, v39
	v_cvt_pk_bf16_f32 v39, v40, v41
	v_cvt_pk_bf16_f32 v40, v34, v35
	v_cvt_pk_bf16_f32 v41, v36, v37
	v_add_u32_e32 v225, 0x30000, v226
	global_store_dwordx4 v225, v[38:41], s[4:5] offset:256
	s_waitcnt vmcnt(17)
	v_lshlrev_b32_e32 v170, 16, v198
	v_and_b32_e32 v198, 0xffff0000, v198
	v_lshlrev_b32_e32 v171, 16, v199
	v_and_b32_e32 v199, 0xffff0000, v199
	v_lshlrev_b32_e32 v214, 16, v200
	v_and_b32_e32 v200, 0xffff0000, v200
	v_lshlrev_b32_e32 v215, 16, v201
	v_and_b32_e32 v201, 0xffff0000, v201
	v_add_f32_e32 v170, v130, v170
	v_add_f32_e32 v198, v131, v198
	v_add_f32_e32 v171, v132, v171
	v_add_f32_e32 v199, v133, v199
	v_add_f32_e32 v214, v122, v214
	v_add_f32_e32 v200, v123, v200
	v_add_f32_e32 v215, v124, v215
	v_add_f32_e32 v201, v125, v201
	v_mul_f32_e32 v170, 0xbfb8aa3b, v170
	v_mul_f32_e32 v198, 0xbfb8aa3b, v198
	v_mul_f32_e32 v171, 0xbfb8aa3b, v171
	v_mul_f32_e32 v199, 0xbfb8aa3b, v199
	v_mul_f32_e32 v214, 0xbfb8aa3b, v214
	v_mul_f32_e32 v200, 0xbfb8aa3b, v200
	v_mul_f32_e32 v215, 0xbfb8aa3b, v215
	v_mul_f32_e32 v201, 0xbfb8aa3b, v201
	v_exp_f32_e32 v170, v170
	v_exp_f32_e32 v198, v198
	v_exp_f32_e32 v171, v171
	v_exp_f32_e32 v199, v199
	v_exp_f32_e32 v214, v214
	v_exp_f32_e32 v200, v200
	v_exp_f32_e32 v215, v215
	v_exp_f32_e32 v201, v201
	v_add_f32_e32 v170, 1.0, v170
	v_add_f32_e32 v198, 1.0, v198
	v_add_f32_e32 v171, 1.0, v171
	v_add_f32_e32 v199, 1.0, v199
	v_add_f32_e32 v214, 1.0, v214
	v_add_f32_e32 v200, 1.0, v200
	v_add_f32_e32 v215, 1.0, v215
	v_add_f32_e32 v201, 1.0, v201
	v_rcp_f32_e32 v170, v170
	v_rcp_f32_e32 v198, v198
	v_rcp_f32_e32 v171, v171
	v_rcp_f32_e32 v199, v199
	v_rcp_f32_e32 v214, v214
	v_rcp_f32_e32 v200, v200
	v_rcp_f32_e32 v215, v215
	v_rcp_f32_e32 v201, v201
	v_fma_f32 v30, v30, v170, v228
	v_fma_f32 v31, v31, v198, v228
	v_fma_f32 v32, v32, v171, v228
	v_fma_f32 v33, v33, v199, v228
	v_fma_f32 v26, v26, v214, v228
	v_fma_f32 v27, v27, v200, v228
	v_fma_f32 v28, v28, v215, v228
	v_fma_f32 v29, v29, v201, v228
	v_cvt_pk_bf16_f32 v30, v30, v31
	v_cvt_pk_bf16_f32 v31, v32, v33
	v_cvt_pk_bf16_f32 v32, v26, v27
	v_cvt_pk_bf16_f32 v33, v28, v29
	v_add_u32_e32 v225, 0x80000, v226
	global_store_dwordx4 v225, v[30:33], s[4:5] offset:256
	s_waitcnt vmcnt(17)
	v_lshlrev_b32_e32 v170, 16, v202
	v_and_b32_e32 v202, 0xffff0000, v202
	v_lshlrev_b32_e32 v171, 16, v203
	v_and_b32_e32 v203, 0xffff0000, v203
	v_lshlrev_b32_e32 v214, 16, v204
	v_and_b32_e32 v204, 0xffff0000, v204
	v_lshlrev_b32_e32 v215, 16, v205
	v_and_b32_e32 v205, 0xffff0000, v205
	v_add_f32_e32 v170, v130, v170
	v_add_f32_e32 v202, v131, v202
	v_add_f32_e32 v171, v132, v171
	v_add_f32_e32 v203, v133, v203
	v_add_f32_e32 v214, v122, v214
	v_add_f32_e32 v204, v123, v204
	v_add_f32_e32 v215, v124, v215
	v_add_f32_e32 v205, v125, v205
	v_mul_f32_e32 v170, 0xbfb8aa3b, v170
	v_mul_f32_e32 v202, 0xbfb8aa3b, v202
	v_mul_f32_e32 v171, 0xbfb8aa3b, v171
	v_mul_f32_e32 v203, 0xbfb8aa3b, v203
	v_mul_f32_e32 v214, 0xbfb8aa3b, v214
	v_mul_f32_e32 v204, 0xbfb8aa3b, v204
	v_mul_f32_e32 v215, 0xbfb8aa3b, v215
	v_mul_f32_e32 v205, 0xbfb8aa3b, v205
	v_exp_f32_e32 v170, v170
	v_exp_f32_e32 v202, v202
	v_exp_f32_e32 v171, v171
	v_exp_f32_e32 v203, v203
	v_exp_f32_e32 v214, v214
	v_exp_f32_e32 v204, v204
	v_exp_f32_e32 v215, v215
	v_exp_f32_e32 v205, v205
	v_add_f32_e32 v170, 1.0, v170
	v_add_f32_e32 v202, 1.0, v202
	v_add_f32_e32 v171, 1.0, v171
	v_add_f32_e32 v203, 1.0, v203
	v_add_f32_e32 v214, 1.0, v214
	v_add_f32_e32 v204, 1.0, v204
	v_add_f32_e32 v215, 1.0, v215
	v_add_f32_e32 v205, 1.0, v205
	v_rcp_f32_e32 v170, v170
	v_rcp_f32_e32 v202, v202
	v_rcp_f32_e32 v171, v171
	v_rcp_f32_e32 v203, v203
	v_rcp_f32_e32 v214, v214
	v_rcp_f32_e32 v204, v204
	v_rcp_f32_e32 v215, v215
	v_rcp_f32_e32 v205, v205
	v_fma_f32 v22, v22, v170, v232
	v_fma_f32 v23, v23, v202, v232
	v_fma_f32 v24, v24, v171, v232
	v_fma_f32 v25, v25, v203, v232
	v_fma_f32 v18, v18, v214, v232
	v_fma_f32 v19, v19, v204, v232
	v_fma_f32 v20, v20, v215, v232
	v_fma_f32 v21, v21, v205, v232
	v_cvt_pk_bf16_f32 v22, v22, v23
	v_cvt_pk_bf16_f32 v23, v24, v25
	v_cvt_pk_bf16_f32 v24, v18, v19
	v_cvt_pk_bf16_f32 v25, v20, v21
	v_add_u32_e32 v225, 0x90000, v226
	global_store_dwordx4 v225, v[22:25], s[4:5] offset:256
	s_waitcnt vmcnt(17)
; __device__ __forceinline__ void unpack8(const v4u w, float (&o)[8]) { o[0] = bflo(w.x); o[1] = bfhi(w.x); o[2] = bflo(w.y); o[3] = bfhi(w.y); o[4] = bflo(w.z); o[5] = bfhi(w.z); o[6] = bflo(w.w); o[7] = bfhi(w.w); }
; __device__ __forceinline__ v4u pack8(const float (&o)[8]) { v4u w; w.x = pk2(o[0], o[1]); w.y = pk2(o[2], o[3]); w.z = pk2(o[4], o[5]); w.w = pk2(o[6], o[7]); return w; }
; __device__ __forceinline__ float sigmf(float x) { return __builtin_amdgcn_rcpf(1.f + __expf(-x)); }
;     __device__ __forceinline__ void operator()(const f32x4 (&acc)[2][2][4][2], const pg8::Unit& u, int wr, int wc, int fr, int fq_in) const {
;     ...
;         for (int bj = 0; bj < 2; ++bj) {
;             const int col = col0 + bj * 128;
;             float b0[8];
;             { const f32x4 t0 = *(const f32x4*)(bg + goff + col), t1 = *(const f32x4*)(bg + goff + col + 4);
; #pragma unroll
;               for (int q = 0; q < 4; ++q) { b0[q] = t0[q]; b0[4 + q] = t1[q]; } }
; #pragma unroll
;             for (int ai = 0; ai < 2; ++ai) {
;                 v4u gw_[4], pw_[4];
; #pragma unroll
;                 for (int m = 0; m < 4; ++m) { const size_t row = (size_t)(row0 + ai * 128 + m * 16);
;                     gw_[m] = *(const v4u*)(Gt + row * (2 * D) + goff + col); pw_[m] = first ? (v4u){0u, 0u, 0u, 0u} : *(const v4u*)(O + row * D + col); }
;                 __builtin_amdgcn_sched_barrier(0);
; #pragma unroll
;                 for (int m = 0; m < 4; ++m) { const size_t row = (size_t)(row0 + ai * 128 + m * 16);
;                     float g0[8], p[8]; unpack8(gw_[m], g0); unpack8(pw_[m], p);
;                     float o[8];
; #pragma unroll
;                     for (int q = 0; q < 4; ++q) { o[q] = p[q] + sigmf(g0[q] + b0[q]) * acc[ai][bj][m][0][q]; o[4 + q] = p[4 + q] + sigmf(g0[4 + q] + b0[4 + q]) * acc[ai][bj][m][1][q]; }
;                     *(v4u*)(O + row * D + col) = pack8(o); }
	v_lshlrev_b32_e32 v170, 16, v206
	v_and_b32_e32 v206, 0xffff0000, v206
	v_lshlrev_b32_e32 v171, 16, v207
	v_and_b32_e32 v207, 0xffff0000, v207
	v_lshlrev_b32_e32 v214, 16, v208
	v_and_b32_e32 v208, 0xffff0000, v208
	v_lshlrev_b32_e32 v215, 16, v209
	v_and_b32_e32 v209, 0xffff0000, v209
	v_add_f32_e32 v170, v130, v170
	v_add_f32_e32 v206, v131, v206
	v_add_f32_e32 v171, v132, v171
	v_add_f32_e32 v207, v133, v207
	v_add_f32_e32 v214, v122, v214
	v_add_f32_e32 v208, v123, v208
	v_add_f32_e32 v215, v124, v215
	v_add_f32_e32 v209, v125, v209
	v_mul_f32_e32 v170, 0xbfb8aa3b, v170
	v_mul_f32_e32 v206, 0xbfb8aa3b, v206
	v_mul_f32_e32 v171, 0xbfb8aa3b, v171
	v_mul_f32_e32 v207, 0xbfb8aa3b, v207
	v_mul_f32_e32 v214, 0xbfb8aa3b, v214
	v_mul_f32_e32 v208, 0xbfb8aa3b, v208
	v_mul_f32_e32 v215, 0xbfb8aa3b, v215
	v_mul_f32_e32 v209, 0xbfb8aa3b, v209
	v_exp_f32_e32 v170, v170
	v_exp_f32_e32 v206, v206
	v_exp_f32_e32 v171, v171
	v_exp_f32_e32 v207, v207
	v_exp_f32_e32 v214, v214
	v_exp_f32_e32 v208, v208
	v_exp_f32_e32 v215, v215
	v_exp_f32_e32 v209, v209
	v_add_f32_e32 v170, 1.0, v170
	v_add_f32_e32 v206, 1.0, v206
	v_add_f32_e32 v171, 1.0, v171
	v_add_f32_e32 v207, 1.0, v207
	v_add_f32_e32 v214, 1.0, v214
	v_add_f32_e32 v208, 1.0, v208
	v_add_f32_e32 v215, 1.0, v215
	v_add_f32_e32 v209, 1.0, v209
	v_rcp_f32_e32 v170, v170
	v_rcp_f32_e32 v206, v206
	v_rcp_f32_e32 v171, v171
	v_rcp_f32_e32 v207, v207
	v_rcp_f32_e32 v214, v214
	v_rcp_f32_e32 v208, v208
	v_rcp_f32_e32 v215, v215
	v_rcp_f32_e32 v209, v209
	v_fma_f32 v14, v14, v170, v236
	v_fma_f32 v15, v15, v206, v236
	v_fma_f32 v16, v16, v171, v236
	v_fma_f32 v17, v17, v207, v236
	v_fma_f32 v10, v10, v214, v236
	v_fma_f32 v11, v11, v208, v236
	v_fma_f32 v12, v12, v215, v236
	v_fma_f32 v13, v13, v209, v236
	v_cvt_pk_bf16_f32 v14, v14, v15
	v_cvt_pk_bf16_f32 v15, v16, v17
	v_cvt_pk_bf16_f32 v16, v10, v11
	v_cvt_pk_bf16_f32 v17, v12, v13
	v_add_u32_e32 v225, 0xa0000, v226
	global_store_dwordx4 v225, v[14:17], s[4:5] offset:256
	s_waitcnt vmcnt(17)
	v_lshlrev_b32_e32 v170, 16, v210
	v_and_b32_e32 v210, 0xffff0000, v210
	v_lshlrev_b32_e32 v171, 16, v211
	v_and_b32_e32 v211, 0xffff0000, v211
	v_lshlrev_b32_e32 v214, 16, v212
	v_and_b32_e32 v212, 0xffff0000, v212
	v_lshlrev_b32_e32 v215, 16, v213
	v_and_b32_e32 v213, 0xffff0000, v213
	v_add_f32_e32 v170, v130, v170
	v_add_f32_e32 v210, v131, v210
	v_add_f32_e32 v171, v132, v171
	v_add_f32_e32 v211, v133, v211
	v_add_f32_e32 v214, v122, v214
	v_add_f32_e32 v212, v123, v212
	v_add_f32_e32 v215, v124, v215
	v_add_f32_e32 v213, v125, v213
	v_mul_f32_e32 v170, 0xbfb8aa3b, v170
	v_mul_f32_e32 v210, 0xbfb8aa3b, v210
	v_mul_f32_e32 v171, 0xbfb8aa3b, v171
	v_mul_f32_e32 v211, 0xbfb8aa3b, v211
	v_mul_f32_e32 v214, 0xbfb8aa3b, v214
	v_mul_f32_e32 v212, 0xbfb8aa3b, v212
	v_mul_f32_e32 v215, 0xbfb8aa3b, v215
	v_mul_f32_e32 v213, 0xbfb8aa3b, v213
	v_exp_f32_e32 v170, v170
	v_exp_f32_e32 v210, v210
	v_exp_f32_e32 v171, v171
	v_exp_f32_e32 v211, v211
	v_exp_f32_e32 v214, v214
	v_exp_f32_e32 v212, v212
	v_exp_f32_e32 v215, v215
	v_exp_f32_e32 v213, v213
	v_add_f32_e32 v170, 1.0, v170
	v_add_f32_e32 v210, 1.0, v210
	v_add_f32_e32 v171, 1.0, v171
	v_add_f32_e32 v211, 1.0, v211
	v_add_f32_e32 v214, 1.0, v214
	v_add_f32_e32 v212, 1.0, v212
	v_add_f32_e32 v215, 1.0, v215
	v_add_f32_e32 v213, 1.0, v213
	v_rcp_f32_e32 v170, v170
	v_rcp_f32_e32 v210, v210
	v_rcp_f32_e32 v171, v171
	v_rcp_f32_e32 v211, v211
	v_rcp_f32_e32 v214, v214
	v_rcp_f32_e32 v212, v212
	v_rcp_f32_e32 v215, v215
	v_rcp_f32_e32 v213, v213
	v_fma_f32 v6, v6, v170, v240
	v_fma_f32 v7, v7, v210, v240
	v_fma_f32 v8, v8, v171, v240
	v_fma_f32 v9, v9, v211, v240
	v_fma_f32 v2, v2, v214, v240
	v_fma_f32 v3, v3, v212, v240
	v_fma_f32 v4, v4, v215, v240
	v_fma_f32 v5, v5, v213, v240
	v_cvt_pk_bf16_f32 v6, v6, v7
	v_cvt_pk_bf16_f32 v7, v8, v9
	v_cvt_pk_bf16_f32 v8, v2, v3
	v_cvt_pk_bf16_f32 v9, v4, v5
	v_add_u32_e32 v225, 0xb0000, v226
	global_store_dwordx4 v225, v[6:9], s[4:5] offset:256
	s_branch .Lepi6_done
.Lepi6_second:
	global_load_dwordx4 v[244:247], v252, s[0:1]
	global_load_dwordx4 v[248:251], v252, s[0:1] offset:16
	global_load_dwordx4 v[114:117], v227, s[98:99] nt
	global_load_dwordx4 v[228:231], v226, s[4:5]
	v_add_u32_e32 v254, 0x4000, v227
	global_load_dwordx4 v[118:121], v254, s[98:99] nt
	v_add_u32_e32 v253, 0x10000, v226
	global_load_dwordx4 v[232:235], v253, s[4:5]
	v_add_u32_e32 v254, 0x8000, v227
	global_load_dwordx4 v[138:141], v254, s[98:99] nt
	v_add_u32_e32 v253, 0x20000, v226
	global_load_dwordx4 v[236:239], v253, s[4:5]
	v_add_u32_e32 v254, 0xc000, v227
	global_load_dwordx4 v[142:145], v254, s[98:99] nt
	v_add_u32_e32 v253, 0x30000, v226
	global_load_dwordx4 v[240:243], v253, s[4:5]
	v_add_u32_e32 v254, 0x10000, v227
	global_load_dwordx4 v[146:149], v254, s[98:99] nt
	v_add_u32_e32 v254, 0x14000, v227
	global_load_dwordx4 v[150:153], v254, s[98:99] nt
	v_add_u32_e32 v254, 0x18000, v227
	global_load_dwordx4 v[154:157], v254, s[98:99] nt
	v_add_u32_e32 v254, 0x1c000, v227
	global_load_dwordx4 v[158:161], v254, s[98:99] nt
	v_add_u32_e32 v254, 0x2000, v227
	global_load_dwordx4 v[162:165], v254, s[98:99] nt
	v_add_u32_e32 v254, 0x6000, v227
	global_load_dwordx4 v[166:169], v254, s[98:99] nt
	v_add_u32_e32 v254, 0xa000, v227
	global_load_dwordx4 v[190:193], v254, s[98:99] nt
	v_add_u32_e32 v254, 0xe000, v227
	global_load_dwordx4 v[194:197], v254, s[98:99] nt
	v_add_u32_e32 v254, 0x12000, v227
	global_load_dwordx4 v[198:201], v254, s[98:99] nt
	v_add_u32_e32 v254, 0x16000, v227
	global_load_dwordx4 v[202:205], v254, s[98:99] nt
	v_add_u32_e32 v254, 0x1a000, v227
	global_load_dwordx4 v[206:209], v254, s[98:99] nt
	v_add_u32_e32 v254, 0x1e000, v227
	global_load_dwordx4 v[210:213], v254, s[98:99] nt
	s_waitcnt vmcnt(20)
; __device__ __forceinline__ void unpack8(const v4u w, float (&o)[8]) { o[0] = bflo(w.x); o[1] = bfhi(w.x); o[2] = bflo(w.y); o[3] = bfhi(w.y); o[4] = bflo(w.z); o[5] = bfhi(w.z); o[6] = bflo(w.w); o[7] = bfhi(w.w); }
; __device__ __forceinline__ v4u pack8(const float (&o)[8]) { v4u w; w.x = pk2(o[0], o[1]); w.y = pk2(o[2], o[3]); w.z = pk2(o[4], o[5]); w.w = pk2(o[6], o[7]); return w; }
; __device__ __forceinline__ float sigmf(float x) { return __builtin_amdgcn_rcpf(1.f + __expf(-x)); }
;     __device__ __forceinline__ void operator()(const f32x4 (&acc)[2][2][4][2], const pg8::Unit& u, int wr, int wc, int fr, int fq_in) const {
;     ...
;             { const f32x4 t0 = *(const f32x4*)(bg + goff + col), t1 = *(const f32x4*)(bg + goff + col + 4);
; #pragma unroll
;               for (int q = 0; q < 4; ++q) { b0[q] = t0[q]; b0[4 + q] = t1[q]; } }
; #pragma unroll
;             for (int ai = 0; ai < 2; ++ai) {
;                 v4u gw_[4], pw_[4];
; #pragma unroll
;                 for (int m = 0; m < 4; ++m) { const size_t row = (size_t)(row0 + ai * 128 + m * 16);
;                     gw_[m] = *(const v4u*)(Gt + row * (2 * D) + goff + col); pw_[m] = first ? (v4u){0u, 0u, 0u, 0u} : *(const v4u*)(O + row * D + col); }
;                 __builtin_amdgcn_sched_barrier(0);
; #pragma unroll
;                 for (int m = 0; m < 4; ++m) { const size_t row = (size_t)(row0 + ai * 128 + m * 16);
;                     float g0[8], p[8]; unpack8(gw_[m], g0); unpack8(pw_[m], p);
;                     float o[8];
; #pragma unroll
;                     for (int q = 0; q < 4; ++q) { o[q] = p[q] + sigmf(g0[q] + b0[q]) * acc[ai][bj][m][0][q]; o[4 + q] = p[4 + q] + sigmf(g0[4 + q] + b0[4 + q]) * acc[ai][bj][m][1][q]; }
;                     *(v4u*)(O + row * D + col) = pack8(o); }
	s_waitcnt vmcnt(19)
	v_lshlrev_b32_e32 v170, 16, v114
	v_and_b32_e32 v114, 0xffff0000, v114
	v_lshlrev_b32_e32 v171, 16, v115
	v_and_b32_e32 v115, 0xffff0000, v115
	v_lshlrev_b32_e32 v214, 16, v116
	v_and_b32_e32 v116, 0xffff0000, v116
	v_lshlrev_b32_e32 v215, 16, v117
	v_and_b32_e32 v117, 0xffff0000, v117
	v_add_f32_e32 v170, v244, v170
	v_add_f32_e32 v114, v245, v114
	v_add_f32_e32 v171, v246, v171
	v_add_f32_e32 v115, v247, v115
	v_add_f32_e32 v214, v248, v214
	v_add_f32_e32 v116, v249, v116
	v_add_f32_e32 v215, v250, v215
	v_add_f32_e32 v117, v251, v117
	v_mul_f32_e32 v170, 0xbfb8aa3b, v170
	v_mul_f32_e32 v114, 0xbfb8aa3b, v114
	v_mul_f32_e32 v171, 0xbfb8aa3b, v171
	v_mul_f32_e32 v115, 0xbfb8aa3b, v115
	v_mul_f32_e32 v214, 0xbfb8aa3b, v214
	v_mul_f32_e32 v116, 0xbfb8aa3b, v116
	v_mul_f32_e32 v215, 0xbfb8aa3b, v215
	v_mul_f32_e32 v117, 0xbfb8aa3b, v117
	v_exp_f32_e32 v170, v170
	v_exp_f32_e32 v114, v114
	v_exp_f32_e32 v171, v171
	v_exp_f32_e32 v115, v115
	v_exp_f32_e32 v214, v214
	v_exp_f32_e32 v116, v116
	v_exp_f32_e32 v215, v215
	v_exp_f32_e32 v117, v117
	v_add_f32_e32 v170, 1.0, v170
	v_add_f32_e32 v114, 1.0, v114
	v_add_f32_e32 v171, 1.0, v171
	v_add_f32_e32 v115, 1.0, v115
	v_add_f32_e32 v214, 1.0, v214
	v_add_f32_e32 v116, 1.0, v116
	v_add_f32_e32 v215, 1.0, v215
	v_add_f32_e32 v117, 1.0, v117
	v_rcp_f32_e32 v170, v170
	v_rcp_f32_e32 v114, v114
	v_rcp_f32_e32 v171, v171
	v_rcp_f32_e32 v115, v115
	v_rcp_f32_e32 v214, v214
	v_rcp_f32_e32 v116, v116
	v_rcp_f32_e32 v215, v215
	v_rcp_f32_e32 v117, v117
	s_waitcnt vmcnt(18)
	v_lshlrev_b32_e32 v221, 16, v228
	v_and_b32_e32 v228, 0xffff0000, v228
	v_lshlrev_b32_e32 v222, 16, v229
	v_and_b32_e32 v229, 0xffff0000, v229
	v_lshlrev_b32_e32 v223, 16, v230
	v_and_b32_e32 v230, 0xffff0000, v230
	v_lshlrev_b32_e32 v224, 16, v231
	v_and_b32_e32 v231, 0xffff0000, v231
	v_fma_f32 v134, v134, v170, v221
	v_fma_f32 v135, v135, v114, v228
	v_fma_f32 v136, v136, v171, v222
	v_fma_f32 v137, v137, v115, v229
	v_fma_f32 v130, v130, v214, v223
	v_fma_f32 v131, v131, v116, v230
	v_fma_f32 v132, v132, v215, v224
	v_fma_f32 v133, v133, v117, v231
	v_cvt_pk_bf16_f32 v134, v134, v135
	v_cvt_pk_bf16_f32 v135, v136, v137
	v_cvt_pk_bf16_f32 v136, v130, v131
	v_cvt_pk_bf16_f32 v137, v132, v133
	v_add_u32_e32 v253, 0x80000, v226
	global_load_dwordx4 v[228:231], v253, s[4:5]
	global_store_dwordx4 v226, v[134:137], s[4:5]
	s_waitcnt vmcnt(19)
	v_lshlrev_b32_e32 v170, 16, v118
	v_and_b32_e32 v118, 0xffff0000, v118
	v_lshlrev_b32_e32 v171, 16, v119
	v_and_b32_e32 v119, 0xffff0000, v119
	v_lshlrev_b32_e32 v214, 16, v120
	v_and_b32_e32 v120, 0xffff0000, v120
	v_lshlrev_b32_e32 v215, 16, v121
	v_and_b32_e32 v121, 0xffff0000, v121
	v_add_f32_e32 v170, v244, v170
	v_add_f32_e32 v118, v245, v118
	v_add_f32_e32 v171, v246, v171
	v_add_f32_e32 v119, v247, v119
	v_add_f32_e32 v214, v248, v214
	v_add_f32_e32 v120, v249, v120
	v_add_f32_e32 v215, v250, v215
	v_add_f32_e32 v121, v251, v121
	v_mul_f32_e32 v170, 0xbfb8aa3b, v170
	v_mul_f32_e32 v118, 0xbfb8aa3b, v118
	v_mul_f32_e32 v171, 0xbfb8aa3b, v171
	v_mul_f32_e32 v119, 0xbfb8aa3b, v119
	v_mul_f32_e32 v214, 0xbfb8aa3b, v214
	v_mul_f32_e32 v120, 0xbfb8aa3b, v120
	v_mul_f32_e32 v215, 0xbfb8aa3b, v215
	v_mul_f32_e32 v121, 0xbfb8aa3b, v121
	v_exp_f32_e32 v170, v170
	v_exp_f32_e32 v118, v118
	v_exp_f32_e32 v171, v171
	v_exp_f32_e32 v119, v119
	v_exp_f32_e32 v214, v214
	v_exp_f32_e32 v120, v120
	v_exp_f32_e32 v215, v215
	v_exp_f32_e32 v121, v121
	v_add_f32_e32 v170, 1.0, v170
	v_add_f32_e32 v118, 1.0, v118
	v_add_f32_e32 v171, 1.0, v171
	v_add_f32_e32 v119, 1.0, v119
	v_add_f32_e32 v214, 1.0, v214
	v_add_f32_e32 v120, 1.0, v120
	v_add_f32_e32 v215, 1.0, v215
	v_add_f32_e32 v121, 1.0, v121
	v_rcp_f32_e32 v170, v170
	v_rcp_f32_e32 v118, v118
	v_rcp_f32_e32 v171, v171
	v_rcp_f32_e32 v119, v119
	v_rcp_f32_e32 v214, v214
	v_rcp_f32_e32 v120, v120
	v_rcp_f32_e32 v215, v215
	v_rcp_f32_e32 v121, v121
	s_waitcnt vmcnt(18)
	v_lshlrev_b32_e32 v221, 16, v232
	v_and_b32_e32 v232, 0xffff0000, v232
	v_lshlrev_b32_e32 v222, 16, v233
	v_and_b32_e32 v233, 0xffff0000, v233
	v_lshlrev_b32_e32 v223, 16, v234
	v_and_b32_e32 v234, 0xffff0000, v234
	v_lshlrev_b32_e32 v224, 16, v235
	v_and_b32_e32 v235, 0xffff0000, v235
	v_fma_f32 v126, v126, v170, v221
	v_fma_f32 v127, v127, v118, v232
	v_fma_f32 v128, v128, v171, v222
	v_fma_f32 v129, v129, v119, v233
	v_fma_f32 v122, v122, v214, v223
	v_fma_f32 v123, v123, v120, v234
	v_fma_f32 v124, v124, v215, v224
	v_fma_f32 v125, v125, v121, v235
	v_cvt_pk_bf16_f32 v126, v126, v127
	v_cvt_pk_bf16_f32 v127, v128, v129
	v_cvt_pk_bf16_f32 v128, v122, v123
	v_cvt_pk_bf16_f32 v129, v124, v125
	v_add_u32_e32 v253, 0x90000, v226
	global_load_dwordx4 v[232:235], v253, s[4:5]
	v_add_u32_e32 v225, 0x10000, v226
	global_store_dwordx4 v225, v[126:129], s[4:5]
	global_load_dwordx4 v[130:133], v252, s[0:1] offset:512
	global_load_dwordx4 v[122:125], v252, s[0:1] offset:528
	s_waitcnt vmcnt(21)
; __device__ __forceinline__ void unpack8(const v4u w, float (&o)[8]) { o[0] = bflo(w.x); o[1] = bfhi(w.x); o[2] = bflo(w.y); o[3] = bfhi(w.y); o[4] = bflo(w.z); o[5] = bfhi(w.z); o[6] = bflo(w.w); o[7] = bfhi(w.w); }
; __device__ __forceinline__ v4u pack8(const float (&o)[8]) { v4u w; w.x = pk2(o[0], o[1]); w.y = pk2(o[2], o[3]); w.z = pk2(o[4], o[5]); w.w = pk2(o[6], o[7]); return w; }
; __device__ __forceinline__ float sigmf(float x) { return __builtin_amdgcn_rcpf(1.f + __expf(-x)); }
;     __device__ __forceinline__ void operator()(const f32x4 (&acc)[2][2][4][2], const pg8::Unit& u, int wr, int wc, int fr, int fq_in) const {
;     ...
;                 for (int m = 0; m < 4; ++m) { const size_t row = (size_t)(row0 + ai * 128 + m * 16);
;                     float g0[8], p[8]; unpack8(gw_[m], g0); unpack8(pw_[m], p);
;                     float o[8];
; #pragma unroll
;                     for (int q = 0; q < 4; ++q) { o[q] = p[q] + sigmf(g0[q] + b0[q]) * acc[ai][bj][m][0][q]; o[4 + q] = p[4 + q] + sigmf(g0[4 + q] + b0[4 + q]) * acc[ai][bj][m][1][q]; }
;                     *(v4u*)(O + row * D + col) = pack8(o); }
	v_lshlrev_b32_e32 v170, 16, v138
	v_and_b32_e32 v138, 0xffff0000, v138
	v_lshlrev_b32_e32 v171, 16, v139
	v_and_b32_e32 v139, 0xffff0000, v139
	v_lshlrev_b32_e32 v214, 16, v140
	v_and_b32_e32 v140, 0xffff0000, v140
	v_lshlrev_b32_e32 v215, 16, v141
	v_and_b32_e32 v141, 0xffff0000, v141
	v_add_f32_e32 v170, v244, v170
	v_add_f32_e32 v138, v245, v138
	v_add_f32_e32 v171, v246, v171
	v_add_f32_e32 v139, v247, v139
	v_add_f32_e32 v214, v248, v214
	v_add_f32_e32 v140, v249, v140
	v_add_f32_e32 v215, v250, v215
	v_add_f32_e32 v141, v251, v141
	v_mul_f32_e32 v170, 0xbfb8aa3b, v170
	v_mul_f32_e32 v138, 0xbfb8aa3b, v138
	v_mul_f32_e32 v171, 0xbfb8aa3b, v171
	v_mul_f32_e32 v139, 0xbfb8aa3b, v139
	v_mul_f32_e32 v214, 0xbfb8aa3b, v214
	v_mul_f32_e32 v140, 0xbfb8aa3b, v140
	v_mul_f32_e32 v215, 0xbfb8aa3b, v215
	v_mul_f32_e32 v141, 0xbfb8aa3b, v141
	v_exp_f32_e32 v170, v170
	v_exp_f32_e32 v138, v138
	v_exp_f32_e32 v171, v171
	v_exp_f32_e32 v139, v139
	v_exp_f32_e32 v214, v214
	v_exp_f32_e32 v140, v140
	v_exp_f32_e32 v215, v215
	v_exp_f32_e32 v141, v141
	v_add_f32_e32 v170, 1.0, v170
	v_add_f32_e32 v138, 1.0, v138
	v_add_f32_e32 v171, 1.0, v171
	v_add_f32_e32 v139, 1.0, v139
	v_add_f32_e32 v214, 1.0, v214
	v_add_f32_e32 v140, 1.0, v140
	v_add_f32_e32 v215, 1.0, v215
	v_add_f32_e32 v141, 1.0, v141
	v_rcp_f32_e32 v170, v170
	v_rcp_f32_e32 v138, v138
	v_rcp_f32_e32 v171, v171
	v_rcp_f32_e32 v139, v139
	v_rcp_f32_e32 v214, v214
	v_rcp_f32_e32 v140, v140
	v_rcp_f32_e32 v215, v215
	v_rcp_f32_e32 v141, v141
	s_waitcnt vmcnt(20)
	v_lshlrev_b32_e32 v221, 16, v236
	v_and_b32_e32 v236, 0xffff0000, v236
	v_lshlrev_b32_e32 v222, 16, v237
	v_and_b32_e32 v237, 0xffff0000, v237
	v_lshlrev_b32_e32 v223, 16, v238
	v_and_b32_e32 v238, 0xffff0000, v238
	v_lshlrev_b32_e32 v224, 16, v239
	v_and_b32_e32 v239, 0xffff0000, v239
	v_fma_f32 v110, v110, v170, v221
	v_fma_f32 v111, v111, v138, v236
	v_fma_f32 v112, v112, v171, v222
	v_fma_f32 v113, v113, v139, v237
	v_fma_f32 v106, v106, v214, v223
	v_fma_f32 v107, v107, v140, v238
	v_fma_f32 v108, v108, v215, v224
	v_fma_f32 v109, v109, v141, v239
	v_cvt_pk_bf16_f32 v110, v110, v111
	v_cvt_pk_bf16_f32 v111, v112, v113
	v_cvt_pk_bf16_f32 v112, v106, v107
	v_cvt_pk_bf16_f32 v113, v108, v109
	v_add_u32_e32 v253, 0xa0000, v226
	global_load_dwordx4 v[236:239], v253, s[4:5]
	v_add_u32_e32 v225, 0x20000, v226
	global_store_dwordx4 v225, v[110:113], s[4:5]
	s_waitcnt vmcnt(21)
	v_lshlrev_b32_e32 v170, 16, v142
	v_and_b32_e32 v142, 0xffff0000, v142
	v_lshlrev_b32_e32 v171, 16, v143
	v_and_b32_e32 v143, 0xffff0000, v143
	v_lshlrev_b32_e32 v214, 16, v144
	v_and_b32_e32 v144, 0xffff0000, v144
	v_lshlrev_b32_e32 v215, 16, v145
	v_and_b32_e32 v145, 0xffff0000, v145
	v_add_f32_e32 v170, v244, v170
	v_add_f32_e32 v142, v245, v142
	v_add_f32_e32 v171, v246, v171
	v_add_f32_e32 v143, v247, v143
	v_add_f32_e32 v214, v248, v214
	v_add_f32_e32 v144, v249, v144
	v_add_f32_e32 v215, v250, v215
	v_add_f32_e32 v145, v251, v145
	v_mul_f32_e32 v170, 0xbfb8aa3b, v170
	v_mul_f32_e32 v142, 0xbfb8aa3b, v142
	v_mul_f32_e32 v171, 0xbfb8aa3b, v171
	v_mul_f32_e32 v143, 0xbfb8aa3b, v143
	v_mul_f32_e32 v214, 0xbfb8aa3b, v214
	v_mul_f32_e32 v144, 0xbfb8aa3b, v144
	v_mul_f32_e32 v215, 0xbfb8aa3b, v215
	v_mul_f32_e32 v145, 0xbfb8aa3b, v145
	v_exp_f32_e32 v170, v170
	v_exp_f32_e32 v142, v142
	v_exp_f32_e32 v171, v171
	v_exp_f32_e32 v143, v143
	v_exp_f32_e32 v214, v214
	v_exp_f32_e32 v144, v144
	v_exp_f32_e32 v215, v215
	v_exp_f32_e32 v145, v145
	v_add_f32_e32 v170, 1.0, v170
	v_add_f32_e32 v142, 1.0, v142
	v_add_f32_e32 v171, 1.0, v171
	v_add_f32_e32 v143, 1.0, v143
	v_add_f32_e32 v214, 1.0, v214
	v_add_f32_e32 v144, 1.0, v144
	v_add_f32_e32 v215, 1.0, v215
	v_add_f32_e32 v145, 1.0, v145
	v_rcp_f32_e32 v170, v170
	v_rcp_f32_e32 v142, v142
	v_rcp_f32_e32 v171, v171
	v_rcp_f32_e32 v143, v143
	v_rcp_f32_e32 v214, v214
	v_rcp_f32_e32 v144, v144
	v_rcp_f32_e32 v215, v215
	v_rcp_f32_e32 v145, v145
	s_waitcnt vmcnt(20)
	v_lshlrev_b32_e32 v221, 16, v240
	v_and_b32_e32 v240, 0xffff0000, v240
	v_lshlrev_b32_e32 v222, 16, v241
	v_and_b32_e32 v241, 0xffff0000, v241
	v_lshlrev_b32_e32 v223, 16, v242
	v_and_b32_e32 v242, 0xffff0000, v242
	v_lshlrev_b32_e32 v224, 16, v243
	v_and_b32_e32 v243, 0xffff0000, v243
	v_fma_f32 v102, v102, v170, v221
	v_fma_f32 v103, v103, v142, v240
	v_fma_f32 v104, v104, v171, v222
	v_fma_f32 v105, v105, v143, v241
	v_fma_f32 v98, v98, v214, v223
	v_fma_f32 v99, v99, v144, v242
	v_fma_f32 v100, v100, v215, v224
	v_fma_f32 v101, v101, v145, v243
	v_cvt_pk_bf16_f32 v102, v102, v103
	v_cvt_pk_bf16_f32 v103, v104, v105
	v_cvt_pk_bf16_f32 v104, v98, v99
	v_cvt_pk_bf16_f32 v105, v100, v101
	v_add_u32_e32 v253, 0xb0000, v226
	global_load_dwordx4 v[240:243], v253, s[4:5]
	v_add_u32_e32 v225, 0x30000, v226
	global_store_dwordx4 v225, v[102:105], s[4:5]
	s_waitcnt vmcnt(21)
	v_lshlrev_b32_e32 v170, 16, v146
	v_and_b32_e32 v146, 0xffff0000, v146
	v_lshlrev_b32_e32 v171, 16, v147
	v_and_b32_e32 v147, 0xffff0000, v147
	v_lshlrev_b32_e32 v214, 16, v148
	v_and_b32_e32 v148, 0xffff0000, v148
	v_lshlrev_b32_e32 v215, 16, v149
	v_and_b32_e32 v149, 0xffff0000, v149
	v_add_f32_e32 v170, v244, v170
	v_add_f32_e32 v146, v245, v146
	v_add_f32_e32 v171, v246, v171
	v_add_f32_e32 v147, v247, v147
	v_add_f32_e32 v214, v248, v214
	v_add_f32_e32 v148, v249, v148
	v_add_f32_e32 v215, v250, v215
	v_add_f32_e32 v149, v251, v149
	v_mul_f32_e32 v170, 0xbfb8aa3b, v170
	v_mul_f32_e32 v146, 0xbfb8aa3b, v146
	v_mul_f32_e32 v171, 0xbfb8aa3b, v171
	v_mul_f32_e32 v147, 0xbfb8aa3b, v147
	v_mul_f32_e32 v214, 0xbfb8aa3b, v214
	v_mul_f32_e32 v148, 0xbfb8aa3b, v148
	v_mul_f32_e32 v215, 0xbfb8aa3b, v215
	v_mul_f32_e32 v149, 0xbfb8aa3b, v149
	v_exp_f32_e32 v170, v170
	v_exp_f32_e32 v146, v146
	v_exp_f32_e32 v171, v171
	v_exp_f32_e32 v147, v147
	v_exp_f32_e32 v214, v214
	v_exp_f32_e32 v148, v148
	v_exp_f32_e32 v215, v215
	v_exp_f32_e32 v149, v149
	v_add_f32_e32 v170, 1.0, v170
	v_add_f32_e32 v146, 1.0, v146
	v_add_f32_e32 v171, 1.0, v171
	v_add_f32_e32 v147, 1.0, v147
	v_add_f32_e32 v214, 1.0, v214
	v_add_f32_e32 v148, 1.0, v148
	v_add_f32_e32 v215, 1.0, v215
	v_add_f32_e32 v149, 1.0, v149
	v_rcp_f32_e32 v170, v170
	v_rcp_f32_e32 v146, v146
	v_rcp_f32_e32 v171, v171
	v_rcp_f32_e32 v147, v147
	v_rcp_f32_e32 v214, v214
	v_rcp_f32_e32 v148, v148
	v_rcp_f32_e32 v215, v215
	v_rcp_f32_e32 v149, v149
	s_waitcnt vmcnt(9)
; __device__ __forceinline__ void unpack8(const v4u w, float (&o)[8]) { o[0] = bflo(w.x); o[1] = bfhi(w.x); o[2] = bflo(w.y); o[3] = bfhi(w.y); o[4] = bflo(w.z); o[5] = bfhi(w.z); o[6] = bflo(w.w); o[7] = bfhi(w.w); }
; __device__ __forceinline__ v4u pack8(const float (&o)[8]) { v4u w; w.x = pk2(o[0], o[1]); w.y = pk2(o[2], o[3]); w.z = pk2(o[4], o[5]); w.w = pk2(o[6], o[7]); return w; }
; __device__ __forceinline__ float sigmf(float x) { return __builtin_amdgcn_rcpf(1.f + __expf(-x)); }
;     __device__ __forceinline__ void operator()(const f32x4 (&acc)[2][2][4][2], const pg8::Unit& u, int wr, int wc, int fr, int fq_in) const {
;     ...
;                 for (int m = 0; m < 4; ++m) { const size_t row = (size_t)(row0 + ai * 128 + m * 16);
;                     float g0[8], p[8]; unpack8(gw_[m], g0); unpack8(pw_[m], p);
;                     float o[8];
; #pragma unroll
;                     for (int q = 0; q < 4; ++q) { o[q] = p[q] + sigmf(g0[q] + b0[q]) * acc[ai][bj][m][0][q]; o[4 + q] = p[4 + q] + sigmf(g0[4 + q] + b0[4 + q]) * acc[ai][bj][m][1][q]; }
;                     *(v4u*)(O + row * D + col) = pack8(o); }
	v_lshlrev_b32_e32 v221, 16, v228
	v_and_b32_e32 v228, 0xffff0000, v228
	v_lshlrev_b32_e32 v222, 16, v229
	v_and_b32_e32 v229, 0xffff0000, v229
	v_lshlrev_b32_e32 v223, 16, v230
	v_and_b32_e32 v230, 0xffff0000, v230
	v_lshlrev_b32_e32 v224, 16, v231
	v_and_b32_e32 v231, 0xffff0000, v231
	v_fma_f32 v94, v94, v170, v221
	v_fma_f32 v95, v95, v146, v228
	v_fma_f32 v96, v96, v171, v222
	v_fma_f32 v97, v97, v147, v229
	v_fma_f32 v90, v90, v214, v223
	v_fma_f32 v91, v91, v148, v230
	v_fma_f32 v92, v92, v215, v224
	v_fma_f32 v93, v93, v149, v231
	v_cvt_pk_bf16_f32 v94, v94, v95
	v_cvt_pk_bf16_f32 v95, v96, v97
	v_cvt_pk_bf16_f32 v96, v90, v91
	v_cvt_pk_bf16_f32 v97, v92, v93
	global_load_dwordx4 v[228:231], v226, s[4:5] offset:256
	v_add_u32_e32 v225, 0x80000, v226
	global_store_dwordx4 v225, v[94:97], s[4:5]
	s_waitcnt vmcnt(22)
	v_lshlrev_b32_e32 v170, 16, v150
	v_and_b32_e32 v150, 0xffff0000, v150
	v_lshlrev_b32_e32 v171, 16, v151
	v_and_b32_e32 v151, 0xffff0000, v151
	v_lshlrev_b32_e32 v214, 16, v152
	v_and_b32_e32 v152, 0xffff0000, v152
	v_lshlrev_b32_e32 v215, 16, v153
	v_and_b32_e32 v153, 0xffff0000, v153
	v_add_f32_e32 v170, v244, v170
	v_add_f32_e32 v150, v245, v150
	v_add_f32_e32 v171, v246, v171
	v_add_f32_e32 v151, v247, v151
	v_add_f32_e32 v214, v248, v214
	v_add_f32_e32 v152, v249, v152
	v_add_f32_e32 v215, v250, v215
	v_add_f32_e32 v153, v251, v153
	v_mul_f32_e32 v170, 0xbfb8aa3b, v170
	v_mul_f32_e32 v150, 0xbfb8aa3b, v150
	v_mul_f32_e32 v171, 0xbfb8aa3b, v171
	v_mul_f32_e32 v151, 0xbfb8aa3b, v151
	v_mul_f32_e32 v214, 0xbfb8aa3b, v214
	v_mul_f32_e32 v152, 0xbfb8aa3b, v152
	v_mul_f32_e32 v215, 0xbfb8aa3b, v215
	v_mul_f32_e32 v153, 0xbfb8aa3b, v153
	v_exp_f32_e32 v170, v170
	v_exp_f32_e32 v150, v150
	v_exp_f32_e32 v171, v171
	v_exp_f32_e32 v151, v151
	v_exp_f32_e32 v214, v214
	v_exp_f32_e32 v152, v152
	v_exp_f32_e32 v215, v215
	v_exp_f32_e32 v153, v153
	v_add_f32_e32 v170, 1.0, v170
	v_add_f32_e32 v150, 1.0, v150
	v_add_f32_e32 v171, 1.0, v171
	v_add_f32_e32 v151, 1.0, v151
	v_add_f32_e32 v214, 1.0, v214
	v_add_f32_e32 v152, 1.0, v152
	v_add_f32_e32 v215, 1.0, v215
	v_add_f32_e32 v153, 1.0, v153
	v_rcp_f32_e32 v170, v170
	v_rcp_f32_e32 v150, v150
	v_rcp_f32_e32 v171, v171
	v_rcp_f32_e32 v151, v151
	v_rcp_f32_e32 v214, v214
	v_rcp_f32_e32 v152, v152
	v_rcp_f32_e32 v215, v215
	v_rcp_f32_e32 v153, v153
	s_waitcnt vmcnt(9)
	v_lshlrev_b32_e32 v221, 16, v232
	v_and_b32_e32 v232, 0xffff0000, v232
	v_lshlrev_b32_e32 v222, 16, v233
	v_and_b32_e32 v233, 0xffff0000, v233
	v_lshlrev_b32_e32 v223, 16, v234
	v_and_b32_e32 v234, 0xffff0000, v234
	v_lshlrev_b32_e32 v224, 16, v235
	v_and_b32_e32 v235, 0xffff0000, v235
	v_fma_f32 v86, v86, v170, v221
	v_fma_f32 v87, v87, v150, v232
	v_fma_f32 v88, v88, v171, v222
	v_fma_f32 v89, v89, v151, v233
	v_fma_f32 v82, v82, v214, v223
	v_fma_f32 v83, v83, v152, v234
	v_fma_f32 v84, v84, v215, v224
	v_fma_f32 v85, v85, v153, v235
	v_cvt_pk_bf16_f32 v86, v86, v87
	v_cvt_pk_bf16_f32 v87, v88, v89
	v_cvt_pk_bf16_f32 v88, v82, v83
	v_cvt_pk_bf16_f32 v89, v84, v85
	v_add_u32_e32 v253, 0x10000, v226
	global_load_dwordx4 v[232:235], v253, s[4:5] offset:256
	v_add_u32_e32 v225, 0x90000, v226
	global_store_dwordx4 v225, v[86:89], s[4:5]
	s_waitcnt vmcnt(23)
	v_lshlrev_b32_e32 v170, 16, v154
	v_and_b32_e32 v154, 0xffff0000, v154
	v_lshlrev_b32_e32 v171, 16, v155
	v_and_b32_e32 v155, 0xffff0000, v155
	v_lshlrev_b32_e32 v214, 16, v156
	v_and_b32_e32 v156, 0xffff0000, v156
	v_lshlrev_b32_e32 v215, 16, v157
	v_and_b32_e32 v157, 0xffff0000, v157
	v_add_f32_e32 v170, v244, v170
	v_add_f32_e32 v154, v245, v154
	v_add_f32_e32 v171, v246, v171
	v_add_f32_e32 v155, v247, v155
	v_add_f32_e32 v214, v248, v214
	v_add_f32_e32 v156, v249, v156
	v_add_f32_e32 v215, v250, v215
	v_add_f32_e32 v157, v251, v157
	v_mul_f32_e32 v170, 0xbfb8aa3b, v170
	v_mul_f32_e32 v154, 0xbfb8aa3b, v154
	v_mul_f32_e32 v171, 0xbfb8aa3b, v171
	v_mul_f32_e32 v155, 0xbfb8aa3b, v155
	v_mul_f32_e32 v214, 0xbfb8aa3b, v214
	v_mul_f32_e32 v156, 0xbfb8aa3b, v156
	v_mul_f32_e32 v215, 0xbfb8aa3b, v215
	v_mul_f32_e32 v157, 0xbfb8aa3b, v157
	v_exp_f32_e32 v170, v170
	v_exp_f32_e32 v154, v154
	v_exp_f32_e32 v171, v171
	v_exp_f32_e32 v155, v155
	v_exp_f32_e32 v214, v214
	v_exp_f32_e32 v156, v156
	v_exp_f32_e32 v215, v215
	v_exp_f32_e32 v157, v157
	v_add_f32_e32 v170, 1.0, v170
	v_add_f32_e32 v154, 1.0, v154
	v_add_f32_e32 v171, 1.0, v171
	v_add_f32_e32 v155, 1.0, v155
	v_add_f32_e32 v214, 1.0, v214
	v_add_f32_e32 v156, 1.0, v156
	v_add_f32_e32 v215, 1.0, v215
	v_add_f32_e32 v157, 1.0, v157
	v_rcp_f32_e32 v170, v170
	v_rcp_f32_e32 v154, v154
	v_rcp_f32_e32 v171, v171
	v_rcp_f32_e32 v155, v155
	v_rcp_f32_e32 v214, v214
	v_rcp_f32_e32 v156, v156
	v_rcp_f32_e32 v215, v215
	v_rcp_f32_e32 v157, v157
	s_waitcnt vmcnt(7)
	v_lshlrev_b32_e32 v221, 16, v236
	v_and_b32_e32 v236, 0xffff0000, v236
	v_lshlrev_b32_e32 v222, 16, v237
	v_and_b32_e32 v237, 0xffff0000, v237
	v_lshlrev_b32_e32 v223, 16, v238
	v_and_b32_e32 v238, 0xffff0000, v238
	v_lshlrev_b32_e32 v224, 16, v239
	v_and_b32_e32 v239, 0xffff0000, v239
	v_fma_f32 v78, v78, v170, v221
	v_fma_f32 v79, v79, v154, v236
	v_fma_f32 v80, v80, v171, v222
	v_fma_f32 v81, v81, v155, v237
	v_fma_f32 v74, v74, v214, v223
	v_fma_f32 v75, v75, v156, v238
	v_fma_f32 v76, v76, v215, v224
	v_fma_f32 v77, v77, v157, v239
	v_cvt_pk_bf16_f32 v78, v78, v79
	v_cvt_pk_bf16_f32 v79, v80, v81
	v_cvt_pk_bf16_f32 v80, v74, v75
	v_cvt_pk_bf16_f32 v81, v76, v77
	v_add_u32_e32 v253, 0x20000, v226
	global_load_dwordx4 v[236:239], v253, s[4:5] offset:256
	v_add_u32_e32 v225, 0xa0000, v226
	global_store_dwordx4 v225, v[78:81], s[4:5]
	s_waitcnt vmcnt(24)
; __device__ __forceinline__ void unpack8(const v4u w, float (&o)[8]) { o[0] = bflo(w.x); o[1] = bfhi(w.x); o[2] = bflo(w.y); o[3] = bfhi(w.y); o[4] = bflo(w.z); o[5] = bfhi(w.z); o[6] = bflo(w.w); o[7] = bfhi(w.w); }
; __device__ __forceinline__ v4u pack8(const float (&o)[8]) { v4u w; w.x = pk2(o[0], o[1]); w.y = pk2(o[2], o[3]); w.z = pk2(o[4], o[5]); w.w = pk2(o[6], o[7]); return w; }
; __device__ __forceinline__ float sigmf(float x) { return __builtin_amdgcn_rcpf(1.f + __expf(-x)); }
;     __device__ __forceinline__ void operator()(const f32x4 (&acc)[2][2][4][2], const pg8::Unit& u, int wr, int wc, int fr, int fq_in) const {
;     ...
;                 for (int m = 0; m < 4; ++m) { const size_t row = (size_t)(row0 + ai * 128 + m * 16);
;                     float g0[8], p[8]; unpack8(gw_[m], g0); unpack8(pw_[m], p);
;                     float o[8];
; #pragma unroll
;                     for (int q = 0; q < 4; ++q) { o[q] = p[q] + sigmf(g0[q] + b0[q]) * acc[ai][bj][m][0][q]; o[4 + q] = p[4 + q] + sigmf(g0[4 + q] + b0[4 + q]) * acc[ai][bj][m][1][q]; }
;                     *(v4u*)(O + row * D + col) = pack8(o); }
	v_lshlrev_b32_e32 v170, 16, v158
	v_and_b32_e32 v158, 0xffff0000, v158
	v_lshlrev_b32_e32 v171, 16, v159
	v_and_b32_e32 v159, 0xffff0000, v159
	v_lshlrev_b32_e32 v214, 16, v160
	v_and_b32_e32 v160, 0xffff0000, v160
	v_lshlrev_b32_e32 v215, 16, v161
	v_and_b32_e32 v161, 0xffff0000, v161
	v_add_f32_e32 v170, v244, v170
	v_add_f32_e32 v158, v245, v158
	v_add_f32_e32 v171, v246, v171
	v_add_f32_e32 v159, v247, v159
	v_add_f32_e32 v214, v248, v214
	v_add_f32_e32 v160, v249, v160
	v_add_f32_e32 v215, v250, v215
	v_add_f32_e32 v161, v251, v161
	v_mul_f32_e32 v170, 0xbfb8aa3b, v170
	v_mul_f32_e32 v158, 0xbfb8aa3b, v158
	v_mul_f32_e32 v171, 0xbfb8aa3b, v171
	v_mul_f32_e32 v159, 0xbfb8aa3b, v159
	v_mul_f32_e32 v214, 0xbfb8aa3b, v214
	v_mul_f32_e32 v160, 0xbfb8aa3b, v160
	v_mul_f32_e32 v215, 0xbfb8aa3b, v215
	v_mul_f32_e32 v161, 0xbfb8aa3b, v161
	v_exp_f32_e32 v170, v170
	v_exp_f32_e32 v158, v158
	v_exp_f32_e32 v171, v171
	v_exp_f32_e32 v159, v159
	v_exp_f32_e32 v214, v214
	v_exp_f32_e32 v160, v160
	v_exp_f32_e32 v215, v215
	v_exp_f32_e32 v161, v161
	v_add_f32_e32 v170, 1.0, v170
	v_add_f32_e32 v158, 1.0, v158
	v_add_f32_e32 v171, 1.0, v171
	v_add_f32_e32 v159, 1.0, v159
	v_add_f32_e32 v214, 1.0, v214
	v_add_f32_e32 v160, 1.0, v160
	v_add_f32_e32 v215, 1.0, v215
	v_add_f32_e32 v161, 1.0, v161
	v_rcp_f32_e32 v170, v170
	v_rcp_f32_e32 v158, v158
	v_rcp_f32_e32 v171, v171
	v_rcp_f32_e32 v159, v159
	v_rcp_f32_e32 v214, v214
	v_rcp_f32_e32 v160, v160
	v_rcp_f32_e32 v215, v215
	v_rcp_f32_e32 v161, v161
	s_waitcnt vmcnt(7)
	v_lshlrev_b32_e32 v221, 16, v240
	v_and_b32_e32 v240, 0xffff0000, v240
	v_lshlrev_b32_e32 v222, 16, v241
	v_and_b32_e32 v241, 0xffff0000, v241
	v_lshlrev_b32_e32 v223, 16, v242
	v_and_b32_e32 v242, 0xffff0000, v242
	v_lshlrev_b32_e32 v224, 16, v243
	v_and_b32_e32 v243, 0xffff0000, v243
	v_fma_f32 v70, v70, v170, v221
	v_fma_f32 v71, v71, v158, v240
	v_fma_f32 v72, v72, v171, v222
	v_fma_f32 v73, v73, v159, v241
	v_fma_f32 v66, v66, v214, v223
	v_fma_f32 v67, v67, v160, v242
	v_fma_f32 v68, v68, v215, v224
	v_fma_f32 v69, v69, v161, v243
	v_cvt_pk_bf16_f32 v70, v70, v71
	v_cvt_pk_bf16_f32 v71, v72, v73
	v_cvt_pk_bf16_f32 v72, v66, v67
	v_cvt_pk_bf16_f32 v73, v68, v69
	v_add_u32_e32 v253, 0x30000, v226
	global_load_dwordx4 v[240:243], v253, s[4:5] offset:256
	v_add_u32_e32 v225, 0xb0000, v226
	global_store_dwordx4 v225, v[70:73], s[4:5]
	s_waitcnt vmcnt(12)
	s_waitcnt vmcnt(25)
	v_lshlrev_b32_e32 v170, 16, v162
	v_and_b32_e32 v162, 0xffff0000, v162
	v_lshlrev_b32_e32 v171, 16, v163
	v_and_b32_e32 v163, 0xffff0000, v163
	v_lshlrev_b32_e32 v214, 16, v164
	v_and_b32_e32 v164, 0xffff0000, v164
	v_lshlrev_b32_e32 v215, 16, v165
	v_and_b32_e32 v165, 0xffff0000, v165
	v_add_f32_e32 v170, v130, v170
	v_add_f32_e32 v162, v131, v162
	v_add_f32_e32 v171, v132, v171
	v_add_f32_e32 v163, v133, v163
	v_add_f32_e32 v214, v122, v214
	v_add_f32_e32 v164, v123, v164
	v_add_f32_e32 v215, v124, v215
	v_add_f32_e32 v165, v125, v165
	v_mul_f32_e32 v170, 0xbfb8aa3b, v170
	v_mul_f32_e32 v162, 0xbfb8aa3b, v162
	v_mul_f32_e32 v171, 0xbfb8aa3b, v171
	v_mul_f32_e32 v163, 0xbfb8aa3b, v163
	v_mul_f32_e32 v214, 0xbfb8aa3b, v214
	v_mul_f32_e32 v164, 0xbfb8aa3b, v164
	v_mul_f32_e32 v215, 0xbfb8aa3b, v215
	v_mul_f32_e32 v165, 0xbfb8aa3b, v165
	v_exp_f32_e32 v170, v170
	v_exp_f32_e32 v162, v162
	v_exp_f32_e32 v171, v171
	v_exp_f32_e32 v163, v163
	v_exp_f32_e32 v214, v214
	v_exp_f32_e32 v164, v164
	v_exp_f32_e32 v215, v215
	v_exp_f32_e32 v165, v165
	v_add_f32_e32 v170, 1.0, v170
	v_add_f32_e32 v162, 1.0, v162
	v_add_f32_e32 v171, 1.0, v171
	v_add_f32_e32 v163, 1.0, v163
	v_add_f32_e32 v214, 1.0, v214
	v_add_f32_e32 v164, 1.0, v164
	v_add_f32_e32 v215, 1.0, v215
	v_add_f32_e32 v165, 1.0, v165
	v_rcp_f32_e32 v170, v170
	v_rcp_f32_e32 v162, v162
	v_rcp_f32_e32 v171, v171
	v_rcp_f32_e32 v163, v163
	v_rcp_f32_e32 v214, v214
	v_rcp_f32_e32 v164, v164
	v_rcp_f32_e32 v215, v215
	v_rcp_f32_e32 v165, v165
	s_waitcnt vmcnt(7)
	v_lshlrev_b32_e32 v221, 16, v228
	v_and_b32_e32 v228, 0xffff0000, v228
	v_lshlrev_b32_e32 v222, 16, v229
	v_and_b32_e32 v229, 0xffff0000, v229
	v_lshlrev_b32_e32 v223, 16, v230
	v_and_b32_e32 v230, 0xffff0000, v230
	v_lshlrev_b32_e32 v224, 16, v231
	v_and_b32_e32 v231, 0xffff0000, v231
	v_fma_f32 v62, v62, v170, v221
	v_fma_f32 v63, v63, v162, v228
	v_fma_f32 v64, v64, v171, v222
	v_fma_f32 v65, v65, v163, v229
	v_fma_f32 v58, v58, v214, v223
	v_fma_f32 v59, v59, v164, v230
	v_fma_f32 v60, v60, v215, v224
	v_fma_f32 v61, v61, v165, v231
	v_cvt_pk_bf16_f32 v62, v62, v63
	v_cvt_pk_bf16_f32 v63, v64, v65
	v_cvt_pk_bf16_f32 v64, v58, v59
	v_cvt_pk_bf16_f32 v65, v60, v61
	v_add_u32_e32 v253, 0x80000, v226
	global_load_dwordx4 v[228:231], v253, s[4:5] offset:256
	global_store_dwordx4 v226, v[62:65], s[4:5] offset:256
	s_waitcnt vmcnt(26)
	v_lshlrev_b32_e32 v170, 16, v166
	v_and_b32_e32 v166, 0xffff0000, v166
	v_lshlrev_b32_e32 v171, 16, v167
	v_and_b32_e32 v167, 0xffff0000, v167
	v_lshlrev_b32_e32 v214, 16, v168
	v_and_b32_e32 v168, 0xffff0000, v168
	v_lshlrev_b32_e32 v215, 16, v169
	v_and_b32_e32 v169, 0xffff0000, v169
	v_add_f32_e32 v170, v130, v170
	v_add_f32_e32 v166, v131, v166
	v_add_f32_e32 v171, v132, v171
	v_add_f32_e32 v167, v133, v167
	v_add_f32_e32 v214, v122, v214
	v_add_f32_e32 v168, v123, v168
	v_add_f32_e32 v215, v124, v215
	v_add_f32_e32 v169, v125, v169
	v_mul_f32_e32 v170, 0xbfb8aa3b, v170
	v_mul_f32_e32 v166, 0xbfb8aa3b, v166
	v_mul_f32_e32 v171, 0xbfb8aa3b, v171
	v_mul_f32_e32 v167, 0xbfb8aa3b, v167
	v_mul_f32_e32 v214, 0xbfb8aa3b, v214
	v_mul_f32_e32 v168, 0xbfb8aa3b, v168
	v_mul_f32_e32 v215, 0xbfb8aa3b, v215
	v_mul_f32_e32 v169, 0xbfb8aa3b, v169
	v_exp_f32_e32 v170, v170
	v_exp_f32_e32 v166, v166
	v_exp_f32_e32 v171, v171
	v_exp_f32_e32 v167, v167
	v_exp_f32_e32 v214, v214
	v_exp_f32_e32 v168, v168
	v_exp_f32_e32 v215, v215
	v_exp_f32_e32 v169, v169
	v_add_f32_e32 v170, 1.0, v170
	v_add_f32_e32 v166, 1.0, v166
	v_add_f32_e32 v171, 1.0, v171
	v_add_f32_e32 v167, 1.0, v167
	v_add_f32_e32 v214, 1.0, v214
	v_add_f32_e32 v168, 1.0, v168
	v_add_f32_e32 v215, 1.0, v215
	v_add_f32_e32 v169, 1.0, v169
	v_rcp_f32_e32 v170, v170
	v_rcp_f32_e32 v166, v166
	v_rcp_f32_e32 v171, v171
	v_rcp_f32_e32 v167, v167
	v_rcp_f32_e32 v214, v214
	v_rcp_f32_e32 v168, v168
	v_rcp_f32_e32 v215, v215
	v_rcp_f32_e32 v169, v169
	s_waitcnt vmcnt(7)
; __device__ __forceinline__ void unpack8(const v4u w, float (&o)[8]) { o[0] = bflo(w.x); o[1] = bfhi(w.x); o[2] = bflo(w.y); o[3] = bfhi(w.y); o[4] = bflo(w.z); o[5] = bfhi(w.z); o[6] = bflo(w.w); o[7] = bfhi(w.w); }
; __device__ __forceinline__ v4u pack8(const float (&o)[8]) { v4u w; w.x = pk2(o[0], o[1]); w.y = pk2(o[2], o[3]); w.z = pk2(o[4], o[5]); w.w = pk2(o[6], o[7]); return w; }
; __device__ __forceinline__ float sigmf(float x) { return __builtin_amdgcn_rcpf(1.f + __expf(-x)); }
;     __device__ __forceinline__ void operator()(const f32x4 (&acc)[2][2][4][2], const pg8::Unit& u, int wr, int wc, int fr, int fq_in) const {
;     ...
;                 for (int m = 0; m < 4; ++m) { const size_t row = (size_t)(row0 + ai * 128 + m * 16);
;                     float g0[8], p[8]; unpack8(gw_[m], g0); unpack8(pw_[m], p);
;                     float o[8];
; #pragma unroll
;                     for (int q = 0; q < 4; ++q) { o[q] = p[q] + sigmf(g0[q] + b0[q]) * acc[ai][bj][m][0][q]; o[4 + q] = p[4 + q] + sigmf(g0[4 + q] + b0[4 + q]) * acc[ai][bj][m][1][q]; }
;                     *(v4u*)(O + row * D + col) = pack8(o); }
	v_lshlrev_b32_e32 v221, 16, v232
	v_and_b32_e32 v232, 0xffff0000, v232
	v_lshlrev_b32_e32 v222, 16, v233
	v_and_b32_e32 v233, 0xffff0000, v233
	v_lshlrev_b32_e32 v223, 16, v234
	v_and_b32_e32 v234, 0xffff0000, v234
	v_lshlrev_b32_e32 v224, 16, v235
	v_and_b32_e32 v235, 0xffff0000, v235
	v_fma_f32 v54, v54, v170, v221
	v_fma_f32 v55, v55, v166, v232
	v_fma_f32 v56, v56, v171, v222
	v_fma_f32 v57, v57, v167, v233
	v_fma_f32 v50, v50, v214, v223
	v_fma_f32 v51, v51, v168, v234
	v_fma_f32 v52, v52, v215, v224
	v_fma_f32 v53, v53, v169, v235
	v_cvt_pk_bf16_f32 v54, v54, v55
	v_cvt_pk_bf16_f32 v55, v56, v57
	v_cvt_pk_bf16_f32 v56, v50, v51
	v_cvt_pk_bf16_f32 v57, v52, v53
	v_add_u32_e32 v253, 0x90000, v226
	global_load_dwordx4 v[232:235], v253, s[4:5] offset:256
	v_add_u32_e32 v225, 0x10000, v226
	global_store_dwordx4 v225, v[54:57], s[4:5] offset:256
	s_waitcnt vmcnt(27)
	v_lshlrev_b32_e32 v170, 16, v190
	v_and_b32_e32 v190, 0xffff0000, v190
	v_lshlrev_b32_e32 v171, 16, v191
	v_and_b32_e32 v191, 0xffff0000, v191
	v_lshlrev_b32_e32 v214, 16, v192
	v_and_b32_e32 v192, 0xffff0000, v192
	v_lshlrev_b32_e32 v215, 16, v193
	v_and_b32_e32 v193, 0xffff0000, v193
	v_add_f32_e32 v170, v130, v170
	v_add_f32_e32 v190, v131, v190
	v_add_f32_e32 v171, v132, v171
	v_add_f32_e32 v191, v133, v191
	v_add_f32_e32 v214, v122, v214
	v_add_f32_e32 v192, v123, v192
	v_add_f32_e32 v215, v124, v215
	v_add_f32_e32 v193, v125, v193
	v_mul_f32_e32 v170, 0xbfb8aa3b, v170
	v_mul_f32_e32 v190, 0xbfb8aa3b, v190
	v_mul_f32_e32 v171, 0xbfb8aa3b, v171
	v_mul_f32_e32 v191, 0xbfb8aa3b, v191
	v_mul_f32_e32 v214, 0xbfb8aa3b, v214
	v_mul_f32_e32 v192, 0xbfb8aa3b, v192
	v_mul_f32_e32 v215, 0xbfb8aa3b, v215
	v_mul_f32_e32 v193, 0xbfb8aa3b, v193
	v_exp_f32_e32 v170, v170
	v_exp_f32_e32 v190, v190
	v_exp_f32_e32 v171, v171
	v_exp_f32_e32 v191, v191
	v_exp_f32_e32 v214, v214
	v_exp_f32_e32 v192, v192
	v_exp_f32_e32 v215, v215
	v_exp_f32_e32 v193, v193
	v_add_f32_e32 v170, 1.0, v170
	v_add_f32_e32 v190, 1.0, v190
	v_add_f32_e32 v171, 1.0, v171
	v_add_f32_e32 v191, 1.0, v191
	v_add_f32_e32 v214, 1.0, v214
	v_add_f32_e32 v192, 1.0, v192
	v_add_f32_e32 v215, 1.0, v215
	v_add_f32_e32 v193, 1.0, v193
	v_rcp_f32_e32 v170, v170
	v_rcp_f32_e32 v190, v190
	v_rcp_f32_e32 v171, v171
	v_rcp_f32_e32 v191, v191
	v_rcp_f32_e32 v214, v214
	v_rcp_f32_e32 v192, v192
	v_rcp_f32_e32 v215, v215
	v_rcp_f32_e32 v193, v193
	s_waitcnt vmcnt(7)
	v_lshlrev_b32_e32 v221, 16, v236
	v_and_b32_e32 v236, 0xffff0000, v236
	v_lshlrev_b32_e32 v222, 16, v237
	v_and_b32_e32 v237, 0xffff0000, v237
	v_lshlrev_b32_e32 v223, 16, v238
	v_and_b32_e32 v238, 0xffff0000, v238
	v_lshlrev_b32_e32 v224, 16, v239
	v_and_b32_e32 v239, 0xffff0000, v239
	v_fma_f32 v46, v46, v170, v221
	v_fma_f32 v47, v47, v190, v236
	v_fma_f32 v48, v48, v171, v222
	v_fma_f32 v49, v49, v191, v237
	v_fma_f32 v42, v42, v214, v223
	v_fma_f32 v43, v43, v192, v238
	v_fma_f32 v44, v44, v215, v224
	v_fma_f32 v45, v45, v193, v239
	v_cvt_pk_bf16_f32 v46, v46, v47
	v_cvt_pk_bf16_f32 v47, v48, v49
	v_cvt_pk_bf16_f32 v48, v42, v43
	v_cvt_pk_bf16_f32 v49, v44, v45
	v_add_u32_e32 v253, 0xa0000, v226
	global_load_dwordx4 v[236:239], v253, s[4:5] offset:256
	v_add_u32_e32 v225, 0x20000, v226
	global_store_dwordx4 v225, v[46:49], s[4:5] offset:256
	s_waitcnt vmcnt(28)
	v_lshlrev_b32_e32 v170, 16, v194
	v_and_b32_e32 v194, 0xffff0000, v194
	v_lshlrev_b32_e32 v171, 16, v195
	v_and_b32_e32 v195, 0xffff0000, v195
	v_lshlrev_b32_e32 v214, 16, v196
	v_and_b32_e32 v196, 0xffff0000, v196
	v_lshlrev_b32_e32 v215, 16, v197
	v_and_b32_e32 v197, 0xffff0000, v197
	v_add_f32_e32 v170, v130, v170
	v_add_f32_e32 v194, v131, v194
	v_add_f32_e32 v171, v132, v171
	v_add_f32_e32 v195, v133, v195
	v_add_f32_e32 v214, v122, v214
	v_add_f32_e32 v196, v123, v196
	v_add_f32_e32 v215, v124, v215
	v_add_f32_e32 v197, v125, v197
	v_mul_f32_e32 v170, 0xbfb8aa3b, v170
	v_mul_f32_e32 v194, 0xbfb8aa3b, v194
	v_mul_f32_e32 v171, 0xbfb8aa3b, v171
	v_mul_f32_e32 v195, 0xbfb8aa3b, v195
	v_mul_f32_e32 v214, 0xbfb8aa3b, v214
	v_mul_f32_e32 v196, 0xbfb8aa3b, v196
	v_mul_f32_e32 v215, 0xbfb8aa3b, v215
	v_mul_f32_e32 v197, 0xbfb8aa3b, v197
	v_exp_f32_e32 v170, v170
	v_exp_f32_e32 v194, v194
	v_exp_f32_e32 v171, v171
	v_exp_f32_e32 v195, v195
	v_exp_f32_e32 v214, v214
	v_exp_f32_e32 v196, v196
	v_exp_f32_e32 v215, v215
	v_exp_f32_e32 v197, v197
	v_add_f32_e32 v170, 1.0, v170
	v_add_f32_e32 v194, 1.0, v194
	v_add_f32_e32 v171, 1.0, v171
	v_add_f32_e32 v195, 1.0, v195
	v_add_f32_e32 v214, 1.0, v214
	v_add_f32_e32 v196, 1.0, v196
	v_add_f32_e32 v215, 1.0, v215
	v_add_f32_e32 v197, 1.0, v197
	v_rcp_f32_e32 v170, v170
	v_rcp_f32_e32 v194, v194
	v_rcp_f32_e32 v171, v171
	v_rcp_f32_e32 v195, v195
	v_rcp_f32_e32 v214, v214
	v_rcp_f32_e32 v196, v196
	v_rcp_f32_e32 v215, v215
	v_rcp_f32_e32 v197, v197
	s_waitcnt vmcnt(7)
	v_lshlrev_b32_e32 v221, 16, v240
	v_and_b32_e32 v240, 0xffff0000, v240
	v_lshlrev_b32_e32 v222, 16, v241
	v_and_b32_e32 v241, 0xffff0000, v241
	v_lshlrev_b32_e32 v223, 16, v242
	v_and_b32_e32 v242, 0xffff0000, v242
	v_lshlrev_b32_e32 v224, 16, v243
	v_and_b32_e32 v243, 0xffff0000, v243
	v_fma_f32 v38, v38, v170, v221
	v_fma_f32 v39, v39, v194, v240
	v_fma_f32 v40, v40, v171, v222
	v_fma_f32 v41, v41, v195, v241
	v_fma_f32 v34, v34, v214, v223
	v_fma_f32 v35, v35, v196, v242
	v_fma_f32 v36, v36, v215, v224
	v_fma_f32 v37, v37, v197, v243
	v_cvt_pk_bf16_f32 v38, v38, v39
	v_cvt_pk_bf16_f32 v39, v40, v41
	v_cvt_pk_bf16_f32 v40, v34, v35
	v_cvt_pk_bf16_f32 v41, v36, v37
	v_add_u32_e32 v253, 0xb0000, v226
	global_load_dwordx4 v[240:243], v253, s[4:5] offset:256
	v_add_u32_e32 v225, 0x30000, v226
	global_store_dwordx4 v225, v[38:41], s[4:5] offset:256
	s_waitcnt vmcnt(29)
; __device__ __forceinline__ void unpack8(const v4u w, float (&o)[8]) { o[0] = bflo(w.x); o[1] = bfhi(w.x); o[2] = bflo(w.y); o[3] = bfhi(w.y); o[4] = bflo(w.z); o[5] = bfhi(w.z); o[6] = bflo(w.w); o[7] = bfhi(w.w); }
; __device__ __forceinline__ v4u pack8(const float (&o)[8]) { v4u w; w.x = pk2(o[0], o[1]); w.y = pk2(o[2], o[3]); w.z = pk2(o[4], o[5]); w.w = pk2(o[6], o[7]); return w; }
; __device__ __forceinline__ float sigmf(float x) { return __builtin_amdgcn_rcpf(1.f + __expf(-x)); }
;     __device__ __forceinline__ void operator()(const f32x4 (&acc)[2][2][4][2], const pg8::Unit& u, int wr, int wc, int fr, int fq_in) const {
;     ...
;                 for (int m = 0; m < 4; ++m) { const size_t row = (size_t)(row0 + ai * 128 + m * 16);
;                     float g0[8], p[8]; unpack8(gw_[m], g0); unpack8(pw_[m], p);
;                     float o[8];
; #pragma unroll
;                     for (int q = 0; q < 4; ++q) { o[q] = p[q] + sigmf(g0[q] + b0[q]) * acc[ai][bj][m][0][q]; o[4 + q] = p[4 + q] + sigmf(g0[4 + q] + b0[4 + q]) * acc[ai][bj][m][1][q]; }
;                     *(v4u*)(O + row * D + col) = pack8(o); }
	v_lshlrev_b32_e32 v170, 16, v198
	v_and_b32_e32 v198, 0xffff0000, v198
	v_lshlrev_b32_e32 v171, 16, v199
	v_and_b32_e32 v199, 0xffff0000, v199
	v_lshlrev_b32_e32 v214, 16, v200
	v_and_b32_e32 v200, 0xffff0000, v200
	v_lshlrev_b32_e32 v215, 16, v201
	v_and_b32_e32 v201, 0xffff0000, v201
	v_add_f32_e32 v170, v130, v170
	v_add_f32_e32 v198, v131, v198
	v_add_f32_e32 v171, v132, v171
	v_add_f32_e32 v199, v133, v199
	v_add_f32_e32 v214, v122, v214
	v_add_f32_e32 v200, v123, v200
	v_add_f32_e32 v215, v124, v215
	v_add_f32_e32 v201, v125, v201
	v_mul_f32_e32 v170, 0xbfb8aa3b, v170
	v_mul_f32_e32 v198, 0xbfb8aa3b, v198
	v_mul_f32_e32 v171, 0xbfb8aa3b, v171
	v_mul_f32_e32 v199, 0xbfb8aa3b, v199
	v_mul_f32_e32 v214, 0xbfb8aa3b, v214
	v_mul_f32_e32 v200, 0xbfb8aa3b, v200
	v_mul_f32_e32 v215, 0xbfb8aa3b, v215
	v_mul_f32_e32 v201, 0xbfb8aa3b, v201
	v_exp_f32_e32 v170, v170
	v_exp_f32_e32 v198, v198
	v_exp_f32_e32 v171, v171
	v_exp_f32_e32 v199, v199
	v_exp_f32_e32 v214, v214
	v_exp_f32_e32 v200, v200
	v_exp_f32_e32 v215, v215
	v_exp_f32_e32 v201, v201
	v_add_f32_e32 v170, 1.0, v170
	v_add_f32_e32 v198, 1.0, v198
	v_add_f32_e32 v171, 1.0, v171
	v_add_f32_e32 v199, 1.0, v199
	v_add_f32_e32 v214, 1.0, v214
	v_add_f32_e32 v200, 1.0, v200
	v_add_f32_e32 v215, 1.0, v215
	v_add_f32_e32 v201, 1.0, v201
	v_rcp_f32_e32 v170, v170
	v_rcp_f32_e32 v198, v198
	v_rcp_f32_e32 v171, v171
	v_rcp_f32_e32 v199, v199
	v_rcp_f32_e32 v214, v214
	v_rcp_f32_e32 v200, v200
	v_rcp_f32_e32 v215, v215
	v_rcp_f32_e32 v201, v201
	s_waitcnt vmcnt(7)
	v_lshlrev_b32_e32 v221, 16, v228
	v_and_b32_e32 v228, 0xffff0000, v228
	v_lshlrev_b32_e32 v222, 16, v229
	v_and_b32_e32 v229, 0xffff0000, v229
	v_lshlrev_b32_e32 v223, 16, v230
	v_and_b32_e32 v230, 0xffff0000, v230
	v_lshlrev_b32_e32 v224, 16, v231
	v_and_b32_e32 v231, 0xffff0000, v231
	v_fma_f32 v30, v30, v170, v221
	v_fma_f32 v31, v31, v198, v228
	v_fma_f32 v32, v32, v171, v222
	v_fma_f32 v33, v33, v199, v229
	v_fma_f32 v26, v26, v214, v223
	v_fma_f32 v27, v27, v200, v230
	v_fma_f32 v28, v28, v215, v224
	v_fma_f32 v29, v29, v201, v231
	v_cvt_pk_bf16_f32 v30, v30, v31
	v_cvt_pk_bf16_f32 v31, v32, v33
	v_cvt_pk_bf16_f32 v32, v26, v27
	v_cvt_pk_bf16_f32 v33, v28, v29
	v_add_u32_e32 v225, 0x80000, v226
	global_store_dwordx4 v225, v[30:33], s[4:5] offset:256
	s_waitcnt vmcnt(29)
	v_lshlrev_b32_e32 v170, 16, v202
	v_and_b32_e32 v202, 0xffff0000, v202
	v_lshlrev_b32_e32 v171, 16, v203
	v_and_b32_e32 v203, 0xffff0000, v203
	v_lshlrev_b32_e32 v214, 16, v204
	v_and_b32_e32 v204, 0xffff0000, v204
	v_lshlrev_b32_e32 v215, 16, v205
	v_and_b32_e32 v205, 0xffff0000, v205
	v_add_f32_e32 v170, v130, v170
	v_add_f32_e32 v202, v131, v202
	v_add_f32_e32 v171, v132, v171
	v_add_f32_e32 v203, v133, v203
	v_add_f32_e32 v214, v122, v214
	v_add_f32_e32 v204, v123, v204
	v_add_f32_e32 v215, v124, v215
	v_add_f32_e32 v205, v125, v205
	v_mul_f32_e32 v170, 0xbfb8aa3b, v170
	v_mul_f32_e32 v202, 0xbfb8aa3b, v202
	v_mul_f32_e32 v171, 0xbfb8aa3b, v171
	v_mul_f32_e32 v203, 0xbfb8aa3b, v203
	v_mul_f32_e32 v214, 0xbfb8aa3b, v214
	v_mul_f32_e32 v204, 0xbfb8aa3b, v204
	v_mul_f32_e32 v215, 0xbfb8aa3b, v215
	v_mul_f32_e32 v205, 0xbfb8aa3b, v205
	v_exp_f32_e32 v170, v170
	v_exp_f32_e32 v202, v202
	v_exp_f32_e32 v171, v171
	v_exp_f32_e32 v203, v203
	v_exp_f32_e32 v214, v214
	v_exp_f32_e32 v204, v204
	v_exp_f32_e32 v215, v215
	v_exp_f32_e32 v205, v205
	v_add_f32_e32 v170, 1.0, v170
	v_add_f32_e32 v202, 1.0, v202
	v_add_f32_e32 v171, 1.0, v171
	v_add_f32_e32 v203, 1.0, v203
	v_add_f32_e32 v214, 1.0, v214
	v_add_f32_e32 v204, 1.0, v204
	v_add_f32_e32 v215, 1.0, v215
	v_add_f32_e32 v205, 1.0, v205
	v_rcp_f32_e32 v170, v170
	v_rcp_f32_e32 v202, v202
	v_rcp_f32_e32 v171, v171
	v_rcp_f32_e32 v203, v203
	v_rcp_f32_e32 v214, v214
	v_rcp_f32_e32 v204, v204
	v_rcp_f32_e32 v215, v215
	v_rcp_f32_e32 v205, v205
	s_waitcnt vmcnt(6)
	v_lshlrev_b32_e32 v221, 16, v232
	v_and_b32_e32 v232, 0xffff0000, v232
	v_lshlrev_b32_e32 v222, 16, v233
	v_and_b32_e32 v233, 0xffff0000, v233
	v_lshlrev_b32_e32 v223, 16, v234
	v_and_b32_e32 v234, 0xffff0000, v234
	v_lshlrev_b32_e32 v224, 16, v235
	v_and_b32_e32 v235, 0xffff0000, v235
	v_fma_f32 v22, v22, v170, v221
	v_fma_f32 v23, v23, v202, v232
	v_fma_f32 v24, v24, v171, v222
	v_fma_f32 v25, v25, v203, v233
	v_fma_f32 v18, v18, v214, v223
	v_fma_f32 v19, v19, v204, v234
	v_fma_f32 v20, v20, v215, v224
	v_fma_f32 v21, v21, v205, v235
	v_cvt_pk_bf16_f32 v22, v22, v23
	v_cvt_pk_bf16_f32 v23, v24, v25
	v_cvt_pk_bf16_f32 v24, v18, v19
	v_cvt_pk_bf16_f32 v25, v20, v21
	v_add_u32_e32 v225, 0x90000, v226
	global_store_dwordx4 v225, v[22:25], s[4:5] offset:256
	s_waitcnt vmcnt(29)
; __device__ __forceinline__ void unpack8(const v4u w, float (&o)[8]) { o[0] = bflo(w.x); o[1] = bfhi(w.x); o[2] = bflo(w.y); o[3] = bfhi(w.y); o[4] = bflo(w.z); o[5] = bfhi(w.z); o[6] = bflo(w.w); o[7] = bfhi(w.w); }
; __device__ __forceinline__ v4u pack8(const float (&o)[8]) { v4u w; w.x = pk2(o[0], o[1]); w.y = pk2(o[2], o[3]); w.z = pk2(o[4], o[5]); w.w = pk2(o[6], o[7]); return w; }
; __device__ __forceinline__ float sigmf(float x) { return __builtin_amdgcn_rcpf(1.f + __expf(-x)); }
;     __device__ __forceinline__ void operator()(const f32x4 (&acc)[2][2][4][2], const pg8::Unit& u, int wr, int wc, int fr, int fq_in) const {
;     ...
;                 for (int m = 0; m < 4; ++m) { const size_t row = (size_t)(row0 + ai * 128 + m * 16);
;                     float g0[8], p[8]; unpack8(gw_[m], g0); unpack8(pw_[m], p);
;                     float o[8];
; #pragma unroll
;                     for (int q = 0; q < 4; ++q) { o[q] = p[q] + sigmf(g0[q] + b0[q]) * acc[ai][bj][m][0][q]; o[4 + q] = p[4 + q] + sigmf(g0[4 + q] + b0[4 + q]) * acc[ai][bj][m][1][q]; }
;                     *(v4u*)(O + row * D + col) = pack8(o); }
	v_lshlrev_b32_e32 v170, 16, v206
	v_and_b32_e32 v206, 0xffff0000, v206
	v_lshlrev_b32_e32 v171, 16, v207
	v_and_b32_e32 v207, 0xffff0000, v207
	v_lshlrev_b32_e32 v214, 16, v208
	v_and_b32_e32 v208, 0xffff0000, v208
	v_lshlrev_b32_e32 v215, 16, v209
	v_and_b32_e32 v209, 0xffff0000, v209
	v_add_f32_e32 v170, v130, v170
	v_add_f32_e32 v206, v131, v206
	v_add_f32_e32 v171, v132, v171
	v_add_f32_e32 v207, v133, v207
	v_add_f32_e32 v214, v122, v214
	v_add_f32_e32 v208, v123, v208
	v_add_f32_e32 v215, v124, v215
	v_add_f32_e32 v209, v125, v209
	v_mul_f32_e32 v170, 0xbfb8aa3b, v170
	v_mul_f32_e32 v206, 0xbfb8aa3b, v206
	v_mul_f32_e32 v171, 0xbfb8aa3b, v171
	v_mul_f32_e32 v207, 0xbfb8aa3b, v207
	v_mul_f32_e32 v214, 0xbfb8aa3b, v214
	v_mul_f32_e32 v208, 0xbfb8aa3b, v208
	v_mul_f32_e32 v215, 0xbfb8aa3b, v215
	v_mul_f32_e32 v209, 0xbfb8aa3b, v209
	v_exp_f32_e32 v170, v170
	v_exp_f32_e32 v206, v206
	v_exp_f32_e32 v171, v171
	v_exp_f32_e32 v207, v207
	v_exp_f32_e32 v214, v214
	v_exp_f32_e32 v208, v208
	v_exp_f32_e32 v215, v215
	v_exp_f32_e32 v209, v209
	v_add_f32_e32 v170, 1.0, v170
	v_add_f32_e32 v206, 1.0, v206
	v_add_f32_e32 v171, 1.0, v171
	v_add_f32_e32 v207, 1.0, v207
	v_add_f32_e32 v214, 1.0, v214
	v_add_f32_e32 v208, 1.0, v208
	v_add_f32_e32 v215, 1.0, v215
	v_add_f32_e32 v209, 1.0, v209
	v_rcp_f32_e32 v170, v170
	v_rcp_f32_e32 v206, v206
	v_rcp_f32_e32 v171, v171
	v_rcp_f32_e32 v207, v207
	v_rcp_f32_e32 v214, v214
	v_rcp_f32_e32 v208, v208
	v_rcp_f32_e32 v215, v215
	v_rcp_f32_e32 v209, v209
	s_waitcnt vmcnt(5)
	v_lshlrev_b32_e32 v221, 16, v236
	v_and_b32_e32 v236, 0xffff0000, v236
	v_lshlrev_b32_e32 v222, 16, v237
	v_and_b32_e32 v237, 0xffff0000, v237
	v_lshlrev_b32_e32 v223, 16, v238
	v_and_b32_e32 v238, 0xffff0000, v238
	v_lshlrev_b32_e32 v224, 16, v239
	v_and_b32_e32 v239, 0xffff0000, v239
	v_fma_f32 v14, v14, v170, v221
	v_fma_f32 v15, v15, v206, v236
	v_fma_f32 v16, v16, v171, v222
	v_fma_f32 v17, v17, v207, v237
	v_fma_f32 v10, v10, v214, v223
	v_fma_f32 v11, v11, v208, v238
	v_fma_f32 v12, v12, v215, v224
	v_fma_f32 v13, v13, v209, v239
	v_cvt_pk_bf16_f32 v14, v14, v15
	v_cvt_pk_bf16_f32 v15, v16, v17
	v_cvt_pk_bf16_f32 v16, v10, v11
	v_cvt_pk_bf16_f32 v17, v12, v13
	v_add_u32_e32 v225, 0xa0000, v226
	global_store_dwordx4 v225, v[14:17], s[4:5] offset:256
	s_waitcnt vmcnt(29)
	v_lshlrev_b32_e32 v170, 16, v210
	v_and_b32_e32 v210, 0xffff0000, v210
	v_lshlrev_b32_e32 v171, 16, v211
	v_and_b32_e32 v211, 0xffff0000, v211
	v_lshlrev_b32_e32 v214, 16, v212
	v_and_b32_e32 v212, 0xffff0000, v212
	v_lshlrev_b32_e32 v215, 16, v213
	v_and_b32_e32 v213, 0xffff0000, v213
	v_add_f32_e32 v170, v130, v170
	v_add_f32_e32 v210, v131, v210
	v_add_f32_e32 v171, v132, v171
	v_add_f32_e32 v211, v133, v211
	v_add_f32_e32 v214, v122, v214
	v_add_f32_e32 v212, v123, v212
	v_add_f32_e32 v215, v124, v215
	v_add_f32_e32 v213, v125, v213
	v_mul_f32_e32 v170, 0xbfb8aa3b, v170
	v_mul_f32_e32 v210, 0xbfb8aa3b, v210
	v_mul_f32_e32 v171, 0xbfb8aa3b, v171
	v_mul_f32_e32 v211, 0xbfb8aa3b, v211
	v_mul_f32_e32 v214, 0xbfb8aa3b, v214
	v_mul_f32_e32 v212, 0xbfb8aa3b, v212
	v_mul_f32_e32 v215, 0xbfb8aa3b, v215
	v_mul_f32_e32 v213, 0xbfb8aa3b, v213
	v_exp_f32_e32 v170, v170
	v_exp_f32_e32 v210, v210
	v_exp_f32_e32 v171, v171
	v_exp_f32_e32 v211, v211
	v_exp_f32_e32 v214, v214
	v_exp_f32_e32 v212, v212
	v_exp_f32_e32 v215, v215
	v_exp_f32_e32 v213, v213
	v_add_f32_e32 v170, 1.0, v170
	v_add_f32_e32 v210, 1.0, v210
	v_add_f32_e32 v171, 1.0, v171
	v_add_f32_e32 v211, 1.0, v211
	v_add_f32_e32 v214, 1.0, v214
	v_add_f32_e32 v212, 1.0, v212
	v_add_f32_e32 v215, 1.0, v215
	v_add_f32_e32 v213, 1.0, v213
	v_rcp_f32_e32 v170, v170
	v_rcp_f32_e32 v210, v210
	v_rcp_f32_e32 v171, v171
	v_rcp_f32_e32 v211, v211
	v_rcp_f32_e32 v214, v214
	v_rcp_f32_e32 v212, v212
	v_rcp_f32_e32 v215, v215
	v_rcp_f32_e32 v213, v213
	s_waitcnt vmcnt(4)
	v_lshlrev_b32_e32 v221, 16, v240
	v_and_b32_e32 v240, 0xffff0000, v240
	v_lshlrev_b32_e32 v222, 16, v241
	v_and_b32_e32 v241, 0xffff0000, v241
	v_lshlrev_b32_e32 v223, 16, v242
	v_and_b32_e32 v242, 0xffff0000, v242
	v_lshlrev_b32_e32 v224, 16, v243
	v_and_b32_e32 v243, 0xffff0000, v243
	v_fma_f32 v6, v6, v170, v221
	v_fma_f32 v7, v7, v210, v240
	v_fma_f32 v8, v8, v171, v222
	v_fma_f32 v9, v9, v211, v241
	v_fma_f32 v2, v2, v214, v223
	v_fma_f32 v3, v3, v212, v242
	v_fma_f32 v4, v4, v215, v224
	v_fma_f32 v5, v5, v213, v243
	v_cvt_pk_bf16_f32 v6, v6, v7
	v_cvt_pk_bf16_f32 v7, v8, v9
	v_cvt_pk_bf16_f32 v8, v2, v3
	v_cvt_pk_bf16_f32 v9, v4, v5
	v_add_u32_e32 v225, 0xb0000, v226
	global_store_dwordx4 v225, v[6:9], s[4:5] offset:256
